# P6/P17 residual-epilogue prefetch + gather s==7 tail de-serialisation (baseline table layout)
# baseline (speedup 1.0000x reference)
.LBB0_61:
	s_or_b64 exec, exec, s[4:5]
	s_cmpk_gt_i32 s90, 0x3fff
	s_waitcnt lgkmcnt(0)
	s_barrier
	s_cbranch_scc1 .LBB0_70
	v_mbcnt_lo_u32_b32 v1, -1, 0
	v_mbcnt_hi_u32_b32 v2, -1, v1
	v_and_b32_e32 v1, 64, v2
	v_add_u32_e32 v3, 64, v1
	v_xor_b32_e32 v1, 1, v2
	v_cmp_lt_i32_e32 vcc, v1, v3
	v_xor_b32_e32 v4, 2, v2
	s_lshl_b32 s0, s89, 13
	v_cndmask_b32_e32 v1, v2, v1, vcc
	v_cmp_lt_i32_e32 vcc, v4, v3
	s_ashr_i32 s91, s90, 31
	s_add_i32 s26, s0, 0
	v_cndmask_b32_e32 v4, v2, v4, vcc
	v_lshlrev_b32_e32 v44, 2, v4
	v_xor_b32_e32 v4, 4, v2
	v_cmp_lt_i32_e32 vcc, v4, v3
	s_lshl_b64 s[20:21], s[90:91], 2
	s_add_u32 s2, s82, s20
	v_cndmask_b32_e32 v4, v2, v4, vcc
	v_lshlrev_b32_e32 v45, 2, v4
	v_xor_b32_e32 v4, 8, v2
	v_cmp_lt_i32_e32 vcc, v4, v3
	s_addc_u32 s3, s83, s21
	s_add_u32 s22, s2, 0x300000
	v_cndmask_b32_e32 v4, v2, v4, vcc
	v_lshlrev_b32_e32 v46, 2, v4
	v_xor_b32_e32 v4, 16, v2
	v_cmp_lt_i32_e32 vcc, v4, v3
	s_addc_u32 s23, s3, 0
	s_lshl_b64 s[2:3], s[90:91], 13
	v_cndmask_b32_e32 v4, v2, v4, vcc
	v_lshlrev_b32_e32 v47, 2, v4
	v_xor_b32_e32 v4, 32, v2
	v_cmp_lt_i32_e32 vcc, v4, v3
	v_mov_b32_e32 v37, s3
	s_mul_i32 s3, s90, 0xc0
	v_cndmask_b32_e32 v2, v2, v4, vcc
	v_lshlrev_b32_e32 v48, 2, v2
	v_and_b32_e32 v2, 7, v0
	v_mul_u32_u24_e32 v34, 24, v2
	v_lshl_or_b32 v2, v204, 4, s2
	s_mul_hi_i32 s2, s90, 0xc0
	v_or_b32_e32 v36, 0x1000, v2
	v_mov_b32_e32 v2, s3
	v_mov_b32_e32 v3, s2
	v_bfe_u32 v6, v0, 3, 3
	s_mov_b32 s2, 0x300000
	v_mov_b32_e32 v35, 0
	v_mad_u64_u32 v[2:3], s[2:3], v6, s2, v[2:3]
	v_readlane_b32 s36, v254, 2
	v_lshl_add_u64 v[2:3], v[2:3], 0, v[34:35]
	v_lshlrev_b32_e32 v4, 4, v204
	v_lshlrev_b32_e32 v5, 7, v204
	s_ashr_i32 s87, s86, 31
	v_readlane_b32 s50, v254, 16
	v_readlane_b32 s51, v254, 17
	v_lshl_add_u64 v[40:41], s[82:83], 0, v[2:3]
	s_mov_b64 s[2:3], 0x5400008
	v_lshlrev_b32_e32 v1, 2, v1
	v_cmp_eq_u32_e64 s[0:1], 0, v204
	s_lshl_b64 s[4:5], s[86:87], 2
	v_lshl_add_u64 v[38:39], s[50:51], 0, v[36:37]
	s_lshl_b64 s[8:9], s[86:87], 13
	v_lshl_add_u64 v[42:43], v[40:41], 0, s[2:3]
	s_mul_hi_i32 s11, s86, 0xc0
	s_mul_i32 s10, s86, 0xc0
	s_mov_b32 s2, 0xda24260
	s_mov_b32 s3, 0x40e00000
	s_mov_b32 s28, 0x800000
	v_mov_b32_e32 v51, 0x42000000
	s_mov_b32 s29, 0xc2fc0000
	v_mov_b32_e32 v52, 0x42800000
	v_not_b32_e32 v53, 63
	v_add_u32_e32 v49, s26, v4
	v_add_u32_e32 v50, s26, v5
	s_mov_b32 s30, s90
	v_readlane_b32 s37, v254, 3
	v_readlane_b32 s38, v254, 4
	v_readlane_b32 s39, v254, 5
	v_readlane_b32 s40, v254, 6
	v_readlane_b32 s41, v254, 7
	v_readlane_b32 s42, v254, 8
	v_readlane_b32 s43, v254, 9
	v_readlane_b32 s44, v254, 10
	v_readlane_b32 s45, v254, 11
	v_readlane_b32 s46, v254, 12
	v_readlane_b32 s47, v254, 13
	v_readlane_b32 s48, v254, 14
	v_readlane_b32 s49, v254, 15
	s_branch .LBB0_64

.LBB0_64:
	global_load_dwordx4 v[2:5], v[38:39], off offset:-4096
	global_load_dwordx4 v[6:9], v[38:39], off offset:-3072
	global_load_dwordx4 v[10:13], v[38:39], off offset:-2048
	global_load_dwordx4 v[14:17], v[38:39], off offset:-1024
	global_load_dwordx4 v[18:21], v[38:39], off
	global_load_dwordx4 v[22:25], v[38:39], off offset:1024
	global_load_dwordx4 v[26:29], v[38:39], off offset:2048
	global_load_dwordx4 v[30:33], v[38:39], off offset:3072
	s_waitcnt vmcnt(7)
	v_max_f32_e64 v34, |v5|, |v5|
	v_max_f32_e64 v54, |v4|, |v4|
	s_waitcnt vmcnt(6)
	v_max_f32_e64 v55, |v9|, |v9|
	v_max_f32_e64 v56, |v8|, |v8|
	s_waitcnt vmcnt(5)
	v_max_f32_e64 v57, |v13|, |v13|
	v_max_f32_e64 v58, |v12|, |v12|
	s_waitcnt vmcnt(4)
	v_max_f32_e64 v59, |v17|, |v17|
	v_max_f32_e64 v60, |v16|, |v16|
	v_max_f32_e32 v34, v54, v34
	v_max_f32_e32 v54, v56, v55
	s_waitcnt vmcnt(3)
	v_max_f32_e64 v61, |v21|, |v21|
	v_max_f32_e64 v62, |v20|, |v20|
	s_waitcnt vmcnt(2)
	v_max_f32_e64 v63, |v25|, |v25|
	v_max_f32_e64 v64, |v24|, |v24|
	v_max_f32_e32 v55, v58, v57
	v_max_f32_e32 v56, v60, v59
	v_max3_f32 v34, |v2|, |v3|, v34
	v_max3_f32 v54, |v6|, |v7|, v54
	s_waitcnt vmcnt(1)
	v_max_f32_e64 v65, |v29|, |v29|
	v_max_f32_e64 v66, |v28|, |v28|
	s_waitcnt vmcnt(0)
	v_max_f32_e64 v67, |v33|, |v33|
	v_max_f32_e64 v68, |v32|, |v32|
	v_max_f32_e32 v57, v62, v61
	v_max_f32_e32 v58, v64, v63
	v_max3_f32 v55, |v10|, |v11|, v55
	v_max3_f32 v56, |v14|, |v15|, v56
	v_max3_f32 v34, v34, 0, v54
	v_max_f32_e32 v59, v66, v65
	v_max_f32_e32 v60, v68, v67
	v_max3_f32 v57, |v18|, |v19|, v57
	v_max3_f32 v58, |v22|, |v23|, v58
	v_max3_f32 v34, v34, v55, v56
	v_max3_f32 v59, |v26|, |v27|, v59
	v_max3_f32 v60, |v30|, |v31|, v60
	v_max3_f32 v34, v34, v57, v58
	v_max3_f32 v34, v34, v59, v60
	ds_bpermute_b32 v54, v1, v34
	s_waitcnt lgkmcnt(0)
	v_max_f32_e32 v54, v54, v54
	v_max_f32_e32 v34, v34, v54
	ds_bpermute_b32 v54, v44, v34
	s_waitcnt lgkmcnt(0)
	v_max_f32_e32 v54, v54, v54
	v_max_f32_e32 v34, v34, v54
	ds_bpermute_b32 v54, v45, v34
	s_waitcnt lgkmcnt(0)
	v_max_f32_e32 v54, v54, v54
	v_max_f32_e32 v34, v34, v54
	ds_bpermute_b32 v54, v46, v34
	s_waitcnt lgkmcnt(0)
	v_max_f32_e32 v54, v54, v54
	v_max_f32_e32 v34, v34, v54
	ds_bpermute_b32 v54, v47, v34
	s_waitcnt lgkmcnt(0)
	v_max_f32_e32 v54, v54, v54
	v_max_f32_e32 v34, v34, v54
	ds_bpermute_b32 v54, v48, v34
	s_waitcnt lgkmcnt(0)
	v_max3_f32 v34, v34, v54, s2
	v_div_scale_f32 v54, s[26:27], v34, v34, s3
	v_rcp_f32_e32 v55, v54
	v_div_scale_f32 v56, vcc, s3, v34, s3
	v_fma_f32 v57, -v54, v55, 1.0
	v_fmac_f32_e32 v55, v57, v55
	v_mul_f32_e32 v57, v56, v55
	v_fma_f32 v58, -v54, v57, v56
	v_fmac_f32_e32 v57, v58, v55
	v_fma_f32 v54, -v54, v57, v56
	v_div_fmas_f32 v54, v54, v55, v57
	v_div_fixup_f32 v34, v54, v34, s3
	v_cmp_gt_f32_e32 vcc, s28, v34
	s_nop 1
	v_cndmask_b32_e64 v54, 0, 32, vcc
	v_ldexp_f32 v34, v34, v54
	v_log_f32_e32 v34, v34
	v_cndmask_b32_e32 v54, 0, v51, vcc
	v_sub_f32_e32 v34, v34, v54
	v_floor_f32_e32 v34, v34
	v_cmp_gt_f32_e32 vcc, s29, v34
	s_nop 1
	v_cndmask_b32_e32 v54, 0, v52, vcc
	v_add_f32_e32 v34, v34, v54
	v_exp_f32_e32 v34, v34
	v_cndmask_b32_e32 v54, 0, v53, vcc
	v_ldexp_f32 v34, v34, v54
	v_pk_mul_f32 v[4:5], v[4:5], v[34:35] op_sel_hi:[1,0]
	v_pk_mul_f32 v[2:3], v[2:3], v[34:35] op_sel_hi:[1,0]
	v_pk_mul_f32 v[8:9], v[8:9], v[34:35] op_sel_hi:[1,0]
	v_pk_mul_f32 v[6:7], v[6:7], v[34:35] op_sel_hi:[1,0]
	v_pk_mul_f32 v[12:13], v[12:13], v[34:35] op_sel_hi:[1,0]
	v_pk_mul_f32 v[10:11], v[10:11], v[34:35] op_sel_hi:[1,0]
	v_pk_mul_f32 v[16:17], v[16:17], v[34:35] op_sel_hi:[1,0]
	v_pk_mul_f32 v[14:15], v[14:15], v[34:35] op_sel_hi:[1,0]
	v_pk_mul_f32 v[20:21], v[20:21], v[34:35] op_sel_hi:[1,0]
	v_pk_mul_f32 v[18:19], v[18:19], v[34:35] op_sel_hi:[1,0]
	v_pk_mul_f32 v[24:25], v[24:25], v[34:35] op_sel_hi:[1,0]
	v_pk_mul_f32 v[22:23], v[22:23], v[34:35] op_sel_hi:[1,0]
	v_pk_mul_f32 v[28:29], v[28:29], v[34:35] op_sel_hi:[1,0]
	v_pk_mul_f32 v[26:27], v[26:27], v[34:35] op_sel_hi:[1,0]
	v_pk_mul_f32 v[32:33], v[32:33], v[34:35] op_sel_hi:[1,0]
	v_pk_mul_f32 v[30:31], v[30:31], v[34:35] op_sel_hi:[1,0]
	ds_write_b128 v49, v[2:5]
	ds_write_b128 v49, v[6:9] offset:1024
	ds_write_b128 v49, v[10:13] offset:2048
	ds_write_b128 v49, v[14:17] offset:3072
	ds_write_b128 v49, v[18:21] offset:4096
	ds_write_b128 v49, v[22:25] offset:5120
	ds_write_b128 v49, v[26:29] offset:6144
	ds_write_b128 v49, v[30:33] offset:7168
	s_waitcnt lgkmcnt(0)
	ds_read_b128 v[18:21], v50
	ds_read_b128 v[22:25], v50 offset:16
	ds_read_b128 v[26:29], v50 offset:32
	ds_read_b128 v[30:33], v50 offset:48
	ds_read_b128 v[54:57], v50 offset:64
	ds_read_b128 v[58:61], v50 offset:80
	ds_read_b128 v[62:65], v50 offset:96
	ds_read_b128 v[66:69], v50 offset:112
	s_waitcnt lgkmcnt(7)
	v_mov_b32_e32 v2, v18
	v_mov_b32_e32 v3, v20
	s_waitcnt lgkmcnt(6)
	v_mov_b32_e32 v4, v22
	v_mov_b32_e32 v5, v24
	s_waitcnt lgkmcnt(5)
	v_mov_b32_e32 v6, v26
	v_mov_b32_e32 v7, v28
	s_waitcnt lgkmcnt(4)
	v_mov_b32_e32 v8, v30
	v_mov_b32_e32 v9, v32
	s_waitcnt lgkmcnt(3)
	v_mov_b32_e32 v10, v54
	v_mov_b32_e32 v11, v56
	s_waitcnt lgkmcnt(2)
	v_mov_b32_e32 v12, v58
	v_mov_b32_e32 v13, v60
	s_waitcnt lgkmcnt(1)
	v_mov_b32_e32 v14, v62
	v_mov_b32_e32 v15, v64
	s_waitcnt lgkmcnt(0)
	v_mov_b32_e32 v16, v66
	v_mov_b32_e32 v17, v68
	v_mov_b32_e32 v18, v19
	v_mov_b32_e32 v19, v21
	v_mov_b32_e32 v20, v23
	v_mov_b32_e32 v21, v25
	v_mov_b32_e32 v22, v27
	v_mov_b32_e32 v23, v29
	v_mov_b32_e32 v24, v31
	v_mov_b32_e32 v25, v33
	v_mov_b32_e32 v26, v55
	v_mov_b32_e32 v27, v57
	v_mov_b32_e32 v28, v59
	v_mov_b32_e32 v29, v61
	v_mov_b32_e32 v30, v63
	v_mov_b32_e32 v31, v65
	v_mov_b32_e32 v32, v67
	v_mov_b32_e32 v33, v69
	v_cvt_scalef32_2xpk16_fp6_f32 v[2:7], v[2:17], v[18:33], 1.0
	global_store_dwordx4 v[42:43], v[2:5], off offset:-8
	global_store_dwordx2 v[42:43], v[6:7], off offset:8
	s_and_saveexec_b64 s[26:27], s[0:1]
	s_cbranch_execz .LBB0_63
	v_div_scale_f32 v2, s[34:35], v34, v34, 1.0
	v_rcp_f32_e32 v3, v2
	v_div_scale_f32 v4, vcc, 1.0, v34, 1.0
	v_fma_f32 v5, -v2, v3, 1.0
	v_fmac_f32_e32 v3, v5, v3
	v_mul_f32_e32 v5, v4, v3
	v_fma_f32 v6, -v2, v5, v4
	v_fmac_f32_e32 v5, v6, v3
	v_fma_f32 v2, -v2, v5, v4
	v_div_fmas_f32 v2, v2, v3, v5
	v_div_fixup_f32 v2, v2, v34, 1.0
	global_store_dword v35, v2, s[22:23]
	s_branch .LBB0_63

.LBB0_68:
	global_load_dwordx4 v[2:5], v[34:35], off offset:-4096
	global_load_dwordx4 v[6:9], v[34:35], off offset:-3072
	global_load_dwordx4 v[10:13], v[34:35], off offset:-2048
	global_load_dwordx4 v[14:17], v[34:35], off offset:-1024
	global_load_dwordx4 v[18:21], v[34:35], off
	global_load_dwordx4 v[22:25], v[34:35], off offset:1024
	global_load_dwordx4 v[26:29], v[34:35], off offset:2048
	global_load_dwordx4 v[30:33], v[34:35], off offset:3072
	s_waitcnt vmcnt(7)
	v_max_f32_e64 v38, |v5|, |v5|
	v_max_f32_e64 v43, |v4|, |v4|
	s_waitcnt vmcnt(6)
	v_max_f32_e64 v51, |v9|, |v9|
	v_max_f32_e64 v52, |v8|, |v8|
	s_waitcnt vmcnt(5)
	v_max_f32_e64 v53, |v13|, |v13|
	v_max_f32_e64 v54, |v12|, |v12|
	s_waitcnt vmcnt(4)
	v_max_f32_e64 v55, |v17|, |v17|
	v_max_f32_e64 v56, |v16|, |v16|
	v_max_f32_e32 v38, v43, v38
	v_max_f32_e32 v43, v52, v51
	s_waitcnt vmcnt(3)
	v_max_f32_e64 v57, |v21|, |v21|
	v_max_f32_e64 v58, |v20|, |v20|
	s_waitcnt vmcnt(2)
	v_max_f32_e64 v59, |v25|, |v25|
	v_max_f32_e64 v60, |v24|, |v24|
	v_max_f32_e32 v51, v54, v53
	v_max_f32_e32 v52, v56, v55
	v_max3_f32 v38, |v2|, |v3|, v38
	v_max3_f32 v43, |v6|, |v7|, v43
	s_waitcnt vmcnt(1)
	v_max_f32_e64 v61, |v29|, |v29|
	v_max_f32_e64 v62, |v28|, |v28|
	s_waitcnt vmcnt(0)
	v_max_f32_e64 v63, |v33|, |v33|
	v_max_f32_e64 v64, |v32|, |v32|
	v_max_f32_e32 v53, v58, v57
	v_max_f32_e32 v54, v60, v59
	v_max3_f32 v51, |v10|, |v11|, v51
	v_max3_f32 v52, |v14|, |v15|, v52
	v_max3_f32 v38, v38, 0, v43
	v_max_f32_e32 v55, v62, v61
	v_max_f32_e32 v56, v64, v63
	v_max3_f32 v53, |v18|, |v19|, v53
	v_max3_f32 v54, |v22|, |v23|, v54
	v_max3_f32 v38, v38, v51, v52
	v_max3_f32 v55, |v26|, |v27|, v55
	v_max3_f32 v56, |v30|, |v31|, v56
	v_max3_f32 v38, v38, v53, v54
	v_max3_f32 v38, v38, v55, v56
	ds_bpermute_b32 v43, v1, v38
	s_waitcnt lgkmcnt(0)
	v_max_f32_e32 v43, v43, v43
	v_max_f32_e32 v38, v38, v43
	ds_bpermute_b32 v43, v44, v38
	s_waitcnt lgkmcnt(0)
	v_max_f32_e32 v43, v43, v43
	v_max_f32_e32 v38, v38, v43
	ds_bpermute_b32 v43, v45, v38
	s_waitcnt lgkmcnt(0)
	v_max_f32_e32 v43, v43, v43
	v_max_f32_e32 v38, v38, v43
	ds_bpermute_b32 v43, v46, v38
	s_waitcnt lgkmcnt(0)
	v_max_f32_e32 v43, v43, v43
	v_max_f32_e32 v38, v38, v43
	ds_bpermute_b32 v43, v47, v38
	s_waitcnt lgkmcnt(0)
	v_max_f32_e32 v43, v43, v43
	v_max_f32_e32 v38, v38, v43
	ds_bpermute_b32 v43, v48, v38
	s_waitcnt lgkmcnt(0)
	v_max3_f32 v38, v38, v43, s2
	v_div_scale_f32 v43, s[22:23], v38, v38, s3
	v_rcp_f32_e32 v51, v43
	v_div_scale_f32 v52, vcc, s3, v38, s3
	v_fma_f32 v53, -v43, v51, 1.0
	v_fmac_f32_e32 v51, v53, v51
	v_mul_f32_e32 v53, v52, v51
	v_fma_f32 v54, -v43, v53, v52
	v_fmac_f32_e32 v53, v54, v51
	v_fma_f32 v43, -v43, v53, v52
	v_div_fmas_f32 v43, v43, v51, v53
	v_div_fixup_f32 v38, v43, v38, s3
	v_cmp_gt_f32_e32 vcc, s26, v38
	s_nop 1
	v_cndmask_b32_e64 v43, 0, 32, vcc
	v_ldexp_f32 v38, v38, v43
	v_log_f32_e32 v38, v38
	v_cndmask_b32_e32 v43, 0, v39, vcc
	v_sub_f32_e32 v38, v38, v43
	v_floor_f32_e32 v38, v38
	v_cmp_gt_f32_e32 vcc, s27, v38
	s_nop 1
	v_cndmask_b32_e32 v43, 0, v40, vcc
	v_add_f32_e32 v38, v38, v43
	v_exp_f32_e32 v38, v38
	v_cndmask_b32_e32 v43, 0, v41, vcc
	v_ldexp_f32 v38, v38, v43
	v_pk_mul_f32 v[4:5], v[4:5], v[38:39] op_sel_hi:[1,0]
	v_pk_mul_f32 v[2:3], v[2:3], v[38:39] op_sel_hi:[1,0]
	v_pk_mul_f32 v[8:9], v[8:9], v[38:39] op_sel_hi:[1,0]
	v_pk_mul_f32 v[6:7], v[6:7], v[38:39] op_sel_hi:[1,0]
	v_pk_mul_f32 v[12:13], v[12:13], v[38:39] op_sel_hi:[1,0]
	v_pk_mul_f32 v[10:11], v[10:11], v[38:39] op_sel_hi:[1,0]
	v_pk_mul_f32 v[16:17], v[16:17], v[38:39] op_sel_hi:[1,0]
	v_pk_mul_f32 v[14:15], v[14:15], v[38:39] op_sel_hi:[1,0]
	v_pk_mul_f32 v[20:21], v[20:21], v[38:39] op_sel_hi:[1,0]
	v_pk_mul_f32 v[18:19], v[18:19], v[38:39] op_sel_hi:[1,0]
	v_pk_mul_f32 v[24:25], v[24:25], v[38:39] op_sel_hi:[1,0]
	v_pk_mul_f32 v[22:23], v[22:23], v[38:39] op_sel_hi:[1,0]
	v_pk_mul_f32 v[28:29], v[28:29], v[38:39] op_sel_hi:[1,0]
	v_pk_mul_f32 v[26:27], v[26:27], v[38:39] op_sel_hi:[1,0]
	v_pk_mul_f32 v[32:33], v[32:33], v[38:39] op_sel_hi:[1,0]
	v_pk_mul_f32 v[30:31], v[30:31], v[38:39] op_sel_hi:[1,0]
	ds_write_b128 v49, v[2:5]
	ds_write_b128 v49, v[6:9] offset:1024
	ds_write_b128 v49, v[10:13] offset:2048
	ds_write_b128 v49, v[14:17] offset:3072
	ds_write_b128 v49, v[18:21] offset:4096
	ds_write_b128 v49, v[22:25] offset:5120
	ds_write_b128 v49, v[26:29] offset:6144
	ds_write_b128 v49, v[30:33] offset:7168
	s_waitcnt lgkmcnt(0)
	ds_read_b128 v[18:21], v50
	ds_read_b128 v[22:25], v50 offset:16
	ds_read_b128 v[26:29], v50 offset:32
	ds_read_b128 v[30:33], v50 offset:48
	ds_read_b128 v[52:55], v50 offset:64
	ds_read_b128 v[56:59], v50 offset:80
	ds_read_b128 v[60:63], v50 offset:96
	ds_read_b128 v[64:67], v50 offset:112
	s_waitcnt lgkmcnt(7)
	v_mov_b32_e32 v2, v18
	v_mov_b32_e32 v3, v20
	s_waitcnt lgkmcnt(6)
	v_mov_b32_e32 v4, v22
	v_mov_b32_e32 v5, v24
	s_waitcnt lgkmcnt(5)
	v_mov_b32_e32 v6, v26
	v_mov_b32_e32 v7, v28
	s_waitcnt lgkmcnt(4)
	v_mov_b32_e32 v8, v30
	v_mov_b32_e32 v9, v32
	s_waitcnt lgkmcnt(3)
	v_mov_b32_e32 v10, v52
	v_mov_b32_e32 v11, v54
	s_waitcnt lgkmcnt(2)
	v_mov_b32_e32 v12, v56
	v_mov_b32_e32 v13, v58
	s_waitcnt lgkmcnt(1)
	v_mov_b32_e32 v14, v60
	v_mov_b32_e32 v15, v62
	s_waitcnt lgkmcnt(0)
	v_mov_b32_e32 v16, v64
	v_mov_b32_e32 v17, v66
	v_mov_b32_e32 v18, v19
	v_mov_b32_e32 v19, v21
	v_mov_b32_e32 v20, v23
	v_mov_b32_e32 v21, v25
	v_mov_b32_e32 v22, v27
	v_mov_b32_e32 v23, v29
	v_mov_b32_e32 v24, v31
	v_mov_b32_e32 v25, v33
	v_mov_b32_e32 v26, v53
	v_mov_b32_e32 v27, v55
	v_mov_b32_e32 v28, v57
	v_mov_b32_e32 v29, v59
	v_mov_b32_e32 v30, v61
	v_mov_b32_e32 v31, v63
	v_mov_b32_e32 v32, v65
	v_mov_b32_e32 v33, v67
	v_cvt_scalef32_2xpk16_fp6_f32 v[2:7], v[2:17], v[18:33], 1.0
	global_store_dwordx4 v[36:37], v[2:5], off offset:-8
	global_store_dwordx2 v[36:37], v[6:7], off offset:8
	s_and_saveexec_b64 s[22:23], s[0:1]
	s_cbranch_execz .LBB0_67
	v_div_scale_f32 v2, s[30:31], v38, v38, 1.0
	v_rcp_f32_e32 v3, v2
	v_div_scale_f32 v4, vcc, 1.0, v38, 1.0
	v_fma_f32 v5, -v2, v3, 1.0
	v_fmac_f32_e32 v3, v5, v3
	v_mul_f32_e32 v5, v4, v3
	v_fma_f32 v6, -v2, v5, v4
	v_fmac_f32_e32 v5, v6, v3
	v_fma_f32 v2, -v2, v5, v4
	v_div_fmas_f32 v2, v2, v3, v5
	v_div_fixup_f32 v2, v2, v38, 1.0
	global_store_dword v42, v2, s[20:21]
	s_branch .LBB0_67

.LBB0_738:
	s_cmp_gt_i32 s94, 10
	s_mov_b32 s64, s92
	s_cselect_b64 s[4:5], -1, 0
	s_xor_b64 s[0:1], s[0:1], -1
	v_writelane_b32 v254, s64, 42
	s_or_b64 s[0:1], s[4:5], s[0:1]
	v_bfe_u32 v1, v0, 3, 3
	v_writelane_b32 v254, s65, 43
	s_and_b64 vcc, exec, s[0:1]
	v_lshrrev_b32_e32 v205, 3, v204
	v_and_b32_e32 v206, 7, v0
	s_mul_i32 s93, s89, 0x3600
	v_lshlrev_b32_e32 v188, 2, v204
	v_and_b32_e32 v210, 4, v0
	v_and_b32_e32 v211, 2, v0
	v_and_b32_e32 v212, 1, v0
	v_lshlrev_b32_e32 v189, 4, v1
	v_mbcnt_lo_u32_b32 v208, -1, 0
	s_cbranch_vccnz .LBB0_761
	s_add_u32 s2, s82, 0x5400000
	s_addc_u32 s28, s83, 0
	s_add_i32 s10, s93, 0
	s_cmp_lt_i32 s90, 0x9000
	s_cselect_b64 s[0:1], -1, 0
	s_ashr_i32 s91, s90, 31
	s_waitcnt vmcnt(0)
	v_add_u32_e32 v2, s10, v189
	s_lshl_b64 s[20:21], s[90:91], 12
	v_add_u32_e32 v116, s10, v188
	v_add_u32_e32 v117, 0x2400, v2
	v_lshl_or_b32 v2, v206, 6, s20
	v_mov_b32_e32 v3, s21
	s_mov_b64 s[10:11], 0xd400020
	v_lshl_add_u64 v[88:89], v[2:3], 0, s[10:11]
	v_lshlrev_b32_e32 v2, 4, v206
	v_lshlrev_b32_e32 v3, 1, v205
	v_or3_b32 v2, s93, v2, v3
	v_add_u32_e32 v2, 0, v2
	v_add_u32_e32 v118, 0x2400, v2
	v_cndmask_b32_e64 v2, 0, 1, s[0:1]
	v_mbcnt_hi_u32_b32 v111, -1, v208
	s_lshl_b64 s[18:19], s[90:91], 9
	s_ashr_i32 s87, s86, 31
	v_cmp_ne_u32_e64 s[0:1], 1, v2
	v_and_b32_e32 v2, 64, v111
	s_mov_b32 s29, 0
	v_mul_u32_u24_e32 v110, 24, v206
	v_cmp_eq_u32_e64 s[4:5], 0, v210
	v_cmp_eq_u32_e64 s[6:7], 0, v211
	v_cmp_eq_u32_e64 s[8:9], 0, v212
	v_or_b32_e32 v86, s18, v188
	v_mov_b32_e32 v87, s19
	s_lshl_b64 s[14:15], s[86:87], 9
	s_lshl_b64 s[16:17], s[86:87], 12
	s_movk_i32 s30, 0xc0
	s_mov_b64 s[22:23], 0x200
	v_xor_b32_e32 v112, 4, v111
	v_add_u32_e32 v113, 64, v2
	v_xor_b32_e32 v114, 2, v111
	v_xor_b32_e32 v115, 1, v111
	s_branch .LBB0_741

.LBB0_746:
	ds_read_b128 v[2:5], v123
	ds_read_b128 v[82:85], v123 offset:128
	v_mov_b32_e32 v94, 0
	v_mov_b32_e32 v96, 0
	v_mov_b32_e32 v98, 0
	s_waitcnt lgkmcnt(0)
	v_and_b32_e32 v6, 0xffff, v2
	v_lshrrev_b32_e32 v2, 16, v2
	v_mad_u32_u24 v6, v6, s30, v110
	v_mad_u32_u24 v2, v2, s30, v110
	global_load_dwordx2 v[10:11], v6, s[26:27] offset:16
	s_nop 0
	global_load_dwordx4 v[6:9], v6, s[26:27]
	s_nop 0
	global_load_dwordx2 v[16:17], v2, s[26:27] offset:16
	global_load_dwordx4 v[12:15], v2, s[26:27]
	v_and_b32_e32 v2, 0xffff, v3
	v_mad_u32_u24 v2, v2, s30, v110
	global_load_dwordx2 v[130:131], v2, s[26:27] offset:16
	global_load_dwordx4 v[126:129], v2, s[26:27]
	v_lshrrev_b32_e32 v2, 16, v3
	v_mad_u32_u24 v2, v2, s30, v110
	global_load_dwordx2 v[136:137], v2, s[26:27] offset:16
	global_load_dwordx4 v[132:135], v2, s[26:27]
	v_and_b32_e32 v2, 0xffff, v4
	v_mad_u32_u24 v2, v2, s30, v110
	global_load_dwordx2 v[142:143], v2, s[26:27] offset:16
	global_load_dwordx4 v[138:141], v2, s[26:27]
	v_lshrrev_b32_e32 v3, 16, v4
	v_and_b32_e32 v2, 0xffff, v5
	v_lshrrev_b32_e32 v4, 16, v5
	v_mad_u32_u24 v3, v3, s30, v110
	v_mad_u32_u24 v2, v2, s30, v110
	v_mad_u32_u24 v4, v4, s30, v110
	global_load_dwordx2 v[148:149], v3, s[26:27] offset:16
	global_load_dwordx4 v[144:147], v3, s[26:27]
	global_load_dwordx2 v[154:155], v2, s[26:27] offset:16
	global_load_dwordx4 v[150:153], v2, s[26:27]
	global_load_dwordx2 v[160:161], v4, s[26:27] offset:16
	global_load_dwordx4 v[156:159], v4, s[26:27]
	v_mov_b32_e32 v102, 0
	v_mov_b32_e32 v104, 0
	v_mov_b32_e32 v100, 0
	v_mov_b32_e32 v106, 0
	v_mov_b32_e32 v108, 0
	v_mov_b32_e32 v107, 0
	v_mov_b32_e32 v109, 0
	v_mov_b32_e32 v103, 0
	v_mov_b32_e32 v105, 0
	v_mov_b32_e32 v99, 0
	v_mov_b32_e32 v101, 0
	v_mov_b32_e32 v95, 0
	v_mov_b32_e32 v97, 0
	s_and_b64 vcc, exec, s[12:13]
	s_waitcnt vmcnt(14)
	v_cvt_scalef32_pk32_bf16_fp6 v[50:65], v[6:11], 1.0
	v_dot2c_f32_bf16_e32 v106, v50, v78
	s_waitcnt vmcnt(12)
	v_cvt_scalef32_pk32_bf16_fp6 v[34:49], v[12:17], 1.0
	v_dot2c_f32_bf16_e32 v102, v34, v78
	v_dot2c_f32_bf16_e32 v104, v35, v79
	s_waitcnt vmcnt(10)
	v_cvt_scalef32_pk32_bf16_fp6 v[18:33], v[126:131], 1.0
	v_dot2c_f32_bf16_e32 v98, v18, v78
	v_dot2c_f32_bf16_e32 v98, v20, v80
	s_waitcnt vmcnt(8)
	v_cvt_scalef32_pk32_bf16_fp6 v[2:17], v[132:137], 1.0
	v_dot2c_f32_bf16_e32 v94, v2, v78
	v_dot2c_f32_bf16_e32 v96, v3, v79
	v_dot2c_f32_bf16_e32 v94, v4, v80
	v_dot2c_f32_bf16_e32 v96, v5, v81
	v_dot2c_f32_bf16_e32 v94, v6, v74
	v_dot2c_f32_bf16_e32 v96, v7, v75
	v_dot2c_f32_bf16_e32 v94, v8, v76
	v_dot2c_f32_bf16_e32 v96, v9, v77
	v_dot2c_f32_bf16_e32 v94, v10, v70
	v_dot2c_f32_bf16_e32 v96, v11, v71
	v_dot2c_f32_bf16_e32 v94, v12, v72
	v_dot2c_f32_bf16_e32 v96, v13, v73
	v_dot2c_f32_bf16_e32 v94, v14, v66
	v_dot2c_f32_bf16_e32 v96, v15, v67
	v_dot2c_f32_bf16_e32 v94, v16, v68
	v_dot2c_f32_bf16_e32 v96, v17, v69
	s_waitcnt vmcnt(6)
	v_cvt_scalef32_pk32_bf16_fp6 v[2:17], v[138:143], 1.0
	v_mov_b32_e32 v18, 0
	v_mov_b32_e32 v20, 0
	v_dot2c_f32_bf16_e32 v18, v2, v78
	v_dot2c_f32_bf16_e32 v20, v3, v79
	v_dot2c_f32_bf16_e32 v18, v4, v80
	v_dot2c_f32_bf16_e32 v20, v5, v81
	v_dot2c_f32_bf16_e32 v18, v6, v74
	v_dot2c_f32_bf16_e32 v20, v7, v75
	v_dot2c_f32_bf16_e32 v18, v8, v76
	v_dot2c_f32_bf16_e32 v20, v9, v77
	v_dot2c_f32_bf16_e32 v18, v10, v70
	v_dot2c_f32_bf16_e32 v20, v11, v71
	v_dot2c_f32_bf16_e32 v18, v12, v72
	v_dot2c_f32_bf16_e32 v20, v13, v73
	v_dot2c_f32_bf16_e32 v18, v14, v66
	v_dot2c_f32_bf16_e32 v20, v15, v67
	v_dot2c_f32_bf16_e32 v98, v22, v74
	v_dot2c_f32_bf16_e32 v18, v16, v68
	v_dot2c_f32_bf16_e32 v20, v17, v69
	s_waitcnt vmcnt(4)
	v_cvt_scalef32_pk32_bf16_fp6 v[2:17], v[144:149], 1.0
	v_mov_b32_e32 v22, 0
	v_dot2c_f32_bf16_e32 v22, v2, v78
	v_and_b32_e32 v2, 0xffff, v82
	v_dot2c_f32_bf16_e32 v102, v36, v80
	v_dot2c_f32_bf16_e32 v104, v37, v81
	v_mad_u32_u24 v2, v2, s30, v110
	v_dot2c_f32_bf16_e32 v102, v38, v74
	v_dot2c_f32_bf16_e32 v104, v39, v75
	global_load_dwordx2 v[38:39], v2, s[26:27] offset:16
	global_load_dwordx4 v[34:37], v2, s[26:27]
	v_dot2c_f32_bf16_e32 v98, v24, v76
	v_mov_b32_e32 v24, 0
	v_dot2c_f32_bf16_e32 v100, v19, v79
	v_dot2c_f32_bf16_e32 v102, v40, v76
	v_dot2c_f32_bf16_e32 v104, v41, v77
	v_dot2c_f32_bf16_e32 v24, v3, v79
	v_lshrrev_b32_e32 v19, 16, v82
	v_dot2c_f32_bf16_e32 v102, v42, v70
	v_dot2c_f32_bf16_e32 v104, v43, v71
	v_dot2c_f32_bf16_e32 v22, v4, v80
	v_dot2c_f32_bf16_e32 v24, v5, v81
	v_mad_u32_u24 v19, v19, s30, v110
	v_dot2c_f32_bf16_e32 v102, v44, v72
	v_dot2c_f32_bf16_e32 v104, v45, v73
	v_dot2c_f32_bf16_e32 v22, v6, v74
	v_dot2c_f32_bf16_e32 v24, v7, v75
	global_load_dwordx2 v[44:45], v19, s[26:27] offset:16
	global_load_dwordx4 v[40:43], v19, s[26:27]
	v_dot2c_f32_bf16_e32 v22, v8, v76
	v_dot2c_f32_bf16_e32 v24, v9, v77
	v_dot2c_f32_bf16_e32 v22, v10, v70
	v_dot2c_f32_bf16_e32 v24, v11, v71
	v_dot2c_f32_bf16_e32 v22, v12, v72
	v_dot2c_f32_bf16_e32 v24, v13, v73
	v_dot2c_f32_bf16_e32 v98, v26, v70
	v_dot2c_f32_bf16_e32 v22, v14, v66
	v_dot2c_f32_bf16_e32 v24, v15, v67
	v_dot2c_f32_bf16_e32 v98, v28, v72
	v_dot2c_f32_bf16_e32 v22, v16, v68
	v_dot2c_f32_bf16_e32 v24, v17, v69
	s_waitcnt vmcnt(6)
	v_cvt_scalef32_pk32_bf16_fp6 v[2:17], v[150:155], 1.0
	v_mov_b32_e32 v26, 0
	v_mov_b32_e32 v28, 0
	v_dot2c_f32_bf16_e32 v26, v2, v78
	v_dot2c_f32_bf16_e32 v28, v3, v79
	v_and_b32_e32 v2, 0xffff, v83
	v_dot2c_f32_bf16_e32 v102, v46, v66
	v_dot2c_f32_bf16_e32 v104, v47, v67
	v_dot2c_f32_bf16_e32 v26, v4, v80
	v_dot2c_f32_bf16_e32 v28, v5, v81
	v_mad_u32_u24 v2, v2, s30, v110
	v_dot2c_f32_bf16_e32 v108, v51, v79
	v_dot2c_f32_bf16_e32 v102, v48, v68
	v_dot2c_f32_bf16_e32 v104, v49, v69
	v_dot2c_f32_bf16_e32 v26, v6, v74
	v_dot2c_f32_bf16_e32 v28, v7, v75
	global_load_dwordx2 v[50:51], v2, s[26:27] offset:16
	global_load_dwordx4 v[46:49], v2, s[26:27]
	v_dot2c_f32_bf16_e32 v26, v8, v76
	v_dot2c_f32_bf16_e32 v28, v9, v77
	v_dot2c_f32_bf16_e32 v26, v10, v70
	v_dot2c_f32_bf16_e32 v28, v11, v71
	v_dot2c_f32_bf16_e32 v26, v12, v72
	v_dot2c_f32_bf16_e32 v28, v13, v73
	v_dot2c_f32_bf16_e32 v26, v14, v66
	v_dot2c_f32_bf16_e32 v28, v15, v67
	v_dot2c_f32_bf16_e32 v98, v30, v66
	v_dot2c_f32_bf16_e32 v26, v16, v68
	v_dot2c_f32_bf16_e32 v28, v17, v69
	s_waitcnt vmcnt(6)
	v_cvt_scalef32_pk32_bf16_fp6 v[2:17], v[156:161], 1.0
	v_mov_b32_e32 v30, 0
	v_dot2c_f32_bf16_e32 v106, v52, v80
	v_dot2c_f32_bf16_e32 v108, v53, v81
	v_dot2c_f32_bf16_e32 v30, v2, v78
	v_lshrrev_b32_e32 v2, 16, v83
	v_dot2c_f32_bf16_e32 v106, v54, v74
	v_dot2c_f32_bf16_e32 v108, v55, v75
	v_mad_u32_u24 v2, v2, s30, v110
	v_dot2c_f32_bf16_e32 v106, v56, v76
	v_dot2c_f32_bf16_e32 v108, v57, v77
	global_load_dwordx2 v[56:57], v2, s[26:27] offset:16
	global_load_dwordx4 v[52:55], v2, s[26:27]
	v_dot2c_f32_bf16_e32 v106, v58, v70
	v_dot2c_f32_bf16_e32 v108, v59, v71
	v_and_b32_e32 v2, 0xffff, v84
	v_dot2c_f32_bf16_e32 v106, v60, v72
	v_dot2c_f32_bf16_e32 v108, v61, v73
	v_mad_u32_u24 v2, v2, s30, v110
	v_dot2c_f32_bf16_e32 v106, v62, v66
	v_dot2c_f32_bf16_e32 v108, v63, v67
	global_load_dwordx2 v[62:63], v2, s[26:27] offset:16
	global_load_dwordx4 v[58:61], v2, s[26:27]
	v_lshrrev_b32_e32 v2, 16, v84
	v_mad_u32_u24 v2, v2, s30, v110
	global_load_dwordx2 v[130:131], v2, s[26:27] offset:16
	global_load_dwordx4 v[126:129], v2, s[26:27]
	v_and_b32_e32 v2, 0xffff, v85
	v_mad_u32_u24 v2, v2, s30, v110
	global_load_dwordx2 v[136:137], v2, s[26:27] offset:16
	global_load_dwordx4 v[132:135], v2, s[26:27]
	v_lshrrev_b32_e32 v2, 16, v85
	v_mad_u32_u24 v2, v2, s30, v110
	global_load_dwordx2 v[142:143], v2, s[26:27] offset:16
	global_load_dwordx4 v[138:141], v2, s[26:27]
	v_dot2c_f32_bf16_e32 v98, v32, v68
	v_mov_b32_e32 v32, 0
	v_dot2c_f32_bf16_e32 v32, v3, v79
	v_dot2c_f32_bf16_e32 v30, v4, v80
	v_dot2c_f32_bf16_e32 v32, v5, v81
	v_dot2c_f32_bf16_e32 v30, v6, v74
	v_dot2c_f32_bf16_e32 v32, v7, v75
	v_dot2c_f32_bf16_e32 v30, v8, v76
	v_dot2c_f32_bf16_e32 v32, v9, v77
	v_dot2c_f32_bf16_e32 v30, v10, v70
	v_dot2c_f32_bf16_e32 v32, v11, v71
	v_dot2c_f32_bf16_e32 v30, v12, v72
	v_dot2c_f32_bf16_e32 v32, v13, v73
	v_dot2c_f32_bf16_e32 v30, v14, v66
	v_dot2c_f32_bf16_e32 v32, v15, v67
	v_dot2c_f32_bf16_e32 v30, v16, v68
	v_dot2c_f32_bf16_e32 v32, v17, v69
	s_waitcnt vmcnt(14)
	v_cvt_scalef32_pk32_bf16_fp6 v[2:17], v[34:39], 1.0
	v_dot2c_f32_bf16_e32 v107, v2, v78
	v_dot2c_f32_bf16_e32 v109, v3, v79
	v_dot2c_f32_bf16_e32 v107, v4, v80
	v_dot2c_f32_bf16_e32 v109, v5, v81
	v_dot2c_f32_bf16_e32 v107, v6, v74
	v_dot2c_f32_bf16_e32 v109, v7, v75
	v_dot2c_f32_bf16_e32 v107, v8, v76
	v_dot2c_f32_bf16_e32 v109, v9, v77
	v_dot2c_f32_bf16_e32 v107, v10, v70
	v_dot2c_f32_bf16_e32 v109, v11, v71
	v_dot2c_f32_bf16_e32 v107, v12, v72
	v_dot2c_f32_bf16_e32 v109, v13, v73
	v_dot2c_f32_bf16_e32 v107, v14, v66
	v_dot2c_f32_bf16_e32 v109, v15, v67
	v_dot2c_f32_bf16_e32 v107, v16, v68
	v_dot2c_f32_bf16_e32 v109, v17, v69
	s_waitcnt vmcnt(12)
	v_cvt_scalef32_pk32_bf16_fp6 v[2:17], v[40:45], 1.0
	v_dot2c_f32_bf16_e32 v103, v2, v78
	v_dot2c_f32_bf16_e32 v105, v3, v79
	v_dot2c_f32_bf16_e32 v103, v4, v80
	v_dot2c_f32_bf16_e32 v105, v5, v81
	v_dot2c_f32_bf16_e32 v103, v6, v74
	v_dot2c_f32_bf16_e32 v105, v7, v75
	v_dot2c_f32_bf16_e32 v103, v8, v76
	v_dot2c_f32_bf16_e32 v105, v9, v77
	v_dot2c_f32_bf16_e32 v103, v10, v70
	v_dot2c_f32_bf16_e32 v105, v11, v71
	v_dot2c_f32_bf16_e32 v103, v12, v72
	v_dot2c_f32_bf16_e32 v105, v13, v73
	v_dot2c_f32_bf16_e32 v103, v14, v66
	v_dot2c_f32_bf16_e32 v105, v15, v67
	v_dot2c_f32_bf16_e32 v103, v16, v68
	v_dot2c_f32_bf16_e32 v105, v17, v69
	s_waitcnt vmcnt(10)
	v_cvt_scalef32_pk32_bf16_fp6 v[2:17], v[46:51], 1.0
	v_dot2c_f32_bf16_e32 v99, v2, v78
	v_dot2c_f32_bf16_e32 v101, v3, v79
	v_dot2c_f32_bf16_e32 v99, v4, v80
	v_dot2c_f32_bf16_e32 v101, v5, v81
	v_dot2c_f32_bf16_e32 v99, v6, v74
	v_dot2c_f32_bf16_e32 v101, v7, v75
	v_dot2c_f32_bf16_e32 v99, v8, v76
	v_dot2c_f32_bf16_e32 v101, v9, v77
	v_dot2c_f32_bf16_e32 v99, v10, v70
	v_dot2c_f32_bf16_e32 v101, v11, v71
	v_dot2c_f32_bf16_e32 v99, v12, v72
	v_dot2c_f32_bf16_e32 v101, v13, v73
	v_dot2c_f32_bf16_e32 v99, v14, v66
	v_dot2c_f32_bf16_e32 v101, v15, v67
	v_dot2c_f32_bf16_e32 v99, v16, v68
	v_dot2c_f32_bf16_e32 v101, v17, v69
	s_waitcnt vmcnt(8)
	v_cvt_scalef32_pk32_bf16_fp6 v[2:17], v[52:57], 1.0
	v_dot2c_f32_bf16_e32 v95, v2, v78
	v_dot2c_f32_bf16_e32 v97, v3, v79
	v_dot2c_f32_bf16_e32 v95, v4, v80
	v_dot2c_f32_bf16_e32 v97, v5, v81
	v_dot2c_f32_bf16_e32 v95, v6, v74
	v_dot2c_f32_bf16_e32 v97, v7, v75
	v_dot2c_f32_bf16_e32 v95, v8, v76
	v_dot2c_f32_bf16_e32 v97, v9, v77
	v_dot2c_f32_bf16_e32 v95, v10, v70
	v_dot2c_f32_bf16_e32 v97, v11, v71
	v_dot2c_f32_bf16_e32 v95, v12, v72
	v_dot2c_f32_bf16_e32 v97, v13, v73
	v_dot2c_f32_bf16_e32 v95, v14, v66
	v_dot2c_f32_bf16_e32 v97, v15, v67
	v_dot2c_f32_bf16_e32 v100, v21, v81
	v_dot2c_f32_bf16_e32 v95, v16, v68
	v_dot2c_f32_bf16_e32 v97, v17, v69
	s_waitcnt vmcnt(6)
	v_cvt_scalef32_pk32_bf16_fp6 v[2:17], v[58:63], 1.0
	v_mov_b32_e32 v19, 0
	v_mov_b32_e32 v21, 0
	v_dot2c_f32_bf16_e32 v19, v2, v78
	v_dot2c_f32_bf16_e32 v21, v3, v79
	v_dot2c_f32_bf16_e32 v19, v4, v80
	v_dot2c_f32_bf16_e32 v21, v5, v81
	v_dot2c_f32_bf16_e32 v19, v6, v74
	v_dot2c_f32_bf16_e32 v21, v7, v75
	v_dot2c_f32_bf16_e32 v19, v8, v76
	v_dot2c_f32_bf16_e32 v21, v9, v77
	v_dot2c_f32_bf16_e32 v19, v10, v70
	v_dot2c_f32_bf16_e32 v21, v11, v71
	v_dot2c_f32_bf16_e32 v19, v12, v72
	v_dot2c_f32_bf16_e32 v21, v13, v73
	v_dot2c_f32_bf16_e32 v100, v23, v75
	v_dot2c_f32_bf16_e32 v19, v14, v66
	v_dot2c_f32_bf16_e32 v21, v15, v67
	v_dot2c_f32_bf16_e32 v100, v25, v77
	v_dot2c_f32_bf16_e32 v19, v16, v68
	v_dot2c_f32_bf16_e32 v21, v17, v69
	s_waitcnt vmcnt(4)
	v_cvt_scalef32_pk32_bf16_fp6 v[2:17], v[126:131], 1.0
	v_mov_b32_e32 v23, 0
	v_mov_b32_e32 v25, 0
	v_dot2c_f32_bf16_e32 v23, v2, v78
	v_dot2c_f32_bf16_e32 v25, v3, v79
	v_dot2c_f32_bf16_e32 v23, v4, v80
	v_dot2c_f32_bf16_e32 v25, v5, v81
	v_dot2c_f32_bf16_e32 v23, v6, v74
	v_dot2c_f32_bf16_e32 v25, v7, v75
	v_dot2c_f32_bf16_e32 v23, v8, v76
	v_dot2c_f32_bf16_e32 v25, v9, v77
	v_dot2c_f32_bf16_e32 v23, v10, v70
	v_dot2c_f32_bf16_e32 v25, v11, v71
	v_dot2c_f32_bf16_e32 v23, v12, v72
	v_dot2c_f32_bf16_e32 v25, v13, v73
	v_dot2c_f32_bf16_e32 v100, v27, v71
	v_dot2c_f32_bf16_e32 v23, v14, v66
	v_dot2c_f32_bf16_e32 v25, v15, v67
	v_dot2c_f32_bf16_e32 v100, v29, v73
	v_dot2c_f32_bf16_e32 v23, v16, v68
	v_dot2c_f32_bf16_e32 v25, v17, v69
	s_waitcnt vmcnt(2)
	v_cvt_scalef32_pk32_bf16_fp6 v[2:17], v[132:137], 1.0
	v_mov_b32_e32 v27, 0
	v_mov_b32_e32 v29, 0
	v_dot2c_f32_bf16_e32 v27, v2, v78
	v_dot2c_f32_bf16_e32 v29, v3, v79
	v_dot2c_f32_bf16_e32 v27, v4, v80
	v_dot2c_f32_bf16_e32 v29, v5, v81
	v_dot2c_f32_bf16_e32 v27, v6, v74
	v_dot2c_f32_bf16_e32 v29, v7, v75
	v_dot2c_f32_bf16_e32 v27, v8, v76
	v_dot2c_f32_bf16_e32 v29, v9, v77
	v_dot2c_f32_bf16_e32 v27, v10, v70
	v_dot2c_f32_bf16_e32 v29, v11, v71
	v_dot2c_f32_bf16_e32 v27, v12, v72
	v_dot2c_f32_bf16_e32 v29, v13, v73
	v_dot2c_f32_bf16_e32 v100, v31, v67
	v_dot2c_f32_bf16_e32 v27, v14, v66
	v_dot2c_f32_bf16_e32 v29, v15, v67
	v_dot2c_f32_bf16_e32 v100, v33, v69
	v_dot2c_f32_bf16_e32 v27, v16, v68
	v_dot2c_f32_bf16_e32 v29, v17, v69
	s_waitcnt vmcnt(0)
	v_cvt_scalef32_pk32_bf16_fp6 v[2:17], v[138:143], 1.0
	v_mov_b32_e32 v31, 0
	v_mov_b32_e32 v33, 0
	v_dot2c_f32_bf16_e32 v31, v2, v78
	v_dot2c_f32_bf16_e32 v33, v3, v79
	v_dot2c_f32_bf16_e32 v31, v4, v80
	v_dot2c_f32_bf16_e32 v33, v5, v81
	v_dot2c_f32_bf16_e32 v31, v6, v74
	v_dot2c_f32_bf16_e32 v33, v7, v75
	v_dot2c_f32_bf16_e32 v31, v8, v76
	v_dot2c_f32_bf16_e32 v33, v9, v77
	v_dot2c_f32_bf16_e32 v31, v10, v70
	v_dot2c_f32_bf16_e32 v33, v11, v71
	v_dot2c_f32_bf16_e32 v31, v12, v72
	v_dot2c_f32_bf16_e32 v33, v13, v73
	v_dot2c_f32_bf16_e32 v31, v14, v66
	v_dot2c_f32_bf16_e32 v33, v15, v67
	v_pk_add_f32 v[8:9], v[104:105], v[102:103]
	v_pk_add_f32 v[10:11], v[24:25], v[22:23]
	v_dot2c_f32_bf16_e32 v31, v16, v68
	v_dot2c_f32_bf16_e32 v33, v17, v69
	v_cndmask_b32_e64 v7, v8, v10, s[4:5]
	v_pk_add_f32 v[14:15], v[100:101], v[98:99]
	v_pk_add_f32 v[16:17], v[28:29], v[26:27]
	v_dot2c_f32_bf16_e32 v106, v64, v68
	v_dot2c_f32_bf16_e32 v108, v65, v69
	v_pk_add_f32 v[4:5], v[20:21], v[18:19]
	ds_bpermute_b32 v12, v119, v7
	v_cndmask_b32_e64 v7, v14, v16, s[4:5]
	v_pk_add_f32 v[20:21], v[96:97], v[94:95]
	v_pk_add_f32 v[22:23], v[32:33], v[30:31]
	v_pk_add_f32 v[2:3], v[108:109], v[106:107]
	ds_bpermute_b32 v18, v119, v7
	v_cndmask_b32_e64 v7, v20, v22, s[4:5]
	v_cndmask_b32_e64 v6, v2, v4, s[4:5]
	ds_bpermute_b32 v24, v119, v7
	v_cndmask_b32_e64 v7, v3, v5, s[4:5]
	ds_bpermute_b32 v6, v119, v6
	ds_bpermute_b32 v7, v119, v7
	v_cndmask_b32_e64 v3, v5, v3, s[4:5]
	v_cndmask_b32_e64 v2, v4, v2, s[4:5]
	v_cndmask_b32_e64 v5, v15, v17, s[4:5]
	ds_bpermute_b32 v19, v119, v5
	s_waitcnt lgkmcnt(1)
	v_pk_add_f32 v[2:3], v[2:3], v[6:7]
	v_cndmask_b32_e64 v7, v9, v11, s[4:5]
	ds_bpermute_b32 v13, v119, v7
	v_cndmask_b32_e64 v7, v21, v23, s[4:5]
	ds_bpermute_b32 v25, v119, v7
	v_cndmask_b32_e64 v9, v11, v9, s[4:5]
	v_cndmask_b32_e64 v8, v10, v8, s[4:5]
	v_cndmask_b32_e64 v11, v23, v21, s[4:5]
	v_cndmask_b32_e64 v10, v22, v20, s[4:5]
	v_cndmask_b32_e64 v5, v17, v15, s[4:5]
	v_cndmask_b32_e64 v4, v16, v14, s[4:5]
	s_waitcnt lgkmcnt(1)
	v_pk_add_f32 v[8:9], v[8:9], v[12:13]
	s_waitcnt lgkmcnt(0)
	v_pk_add_f32 v[10:11], v[10:11], v[24:25]
	v_pk_add_f32 v[4:5], v[4:5], v[18:19]
	v_cndmask_b32_e64 v7, v8, v10, s[6:7]
	v_cndmask_b32_e64 v6, v2, v4, s[6:7]
	ds_bpermute_b32 v12, v120, v7
	v_cndmask_b32_e64 v7, v3, v5, s[6:7]
	v_cndmask_b32_e64 v3, v5, v3, s[6:7]
	v_cndmask_b32_e64 v5, v9, v11, s[6:7]
	ds_bpermute_b32 v6, v120, v6
	ds_bpermute_b32 v7, v120, v7
	ds_bpermute_b32 v13, v120, v5
	v_cndmask_b32_e64 v2, v4, v2, s[6:7]
	v_cndmask_b32_e64 v5, v11, v9, s[6:7]
	v_cndmask_b32_e64 v4, v10, v8, s[6:7]
	s_waitcnt lgkmcnt(1)
	v_pk_add_f32 v[2:3], v[2:3], v[6:7]
	s_waitcnt lgkmcnt(0)
	v_pk_add_f32 v[4:5], v[4:5], v[12:13]
	s_nop 0
	v_cndmask_b32_e64 v6, v2, v4, s[8:9]
	v_cndmask_b32_e64 v7, v3, v5, s[8:9]
	ds_bpermute_b32 v6, v121, v6
	ds_bpermute_b32 v7, v121, v7
	v_cndmask_b32_e64 v3, v5, v3, s[8:9]
	v_cndmask_b32_e64 v2, v4, v2, s[8:9]
	s_waitcnt lgkmcnt(0)
	v_pk_add_f32 v[2:3], v[2:3], v[6:7]
	s_cbranch_vccnz .LBB0_743
	ds_read2st64_b32 v[4:5], v124 offset1:1
	s_waitcnt lgkmcnt(0)
	v_pk_add_f32 v[2:3], v[2:3], v[4:5]
	s_branch .LBB0_743

.LBB0_756:
	v_add_u32_e32 v2, s93, v125
	ds_read_b128 v[14:17], v2
	ds_read_b128 v[164:167], v2 offset:128
	v_add_u32_e32 v95, s93, v123
	s_cmp_lt_i32 s40, 0x8000
	s_cselect_b64 s[30:31], -1, 0
	s_waitcnt lgkmcnt(0)
	v_and_b32_e32 v2, 0xffff, v14
	v_lshrrev_b32_e32 v3, 16, v14
	v_and_b32_e32 v14, 0xffff, v15
	v_mad_u32_u24 v2, v2, s21, v110
	v_mad_u32_u24 v8, v3, s21, v110
	v_mad_u32_u24 v14, v14, s21, v110
	global_load_dwordx2 v[6:7], v2, s[26:27] offset:16
	s_nop 0
	global_load_dwordx4 v[2:5], v2, s[26:27]
	s_nop 0
	global_load_dwordx2 v[12:13], v8, s[26:27] offset:16
	s_nop 0
	global_load_dwordx4 v[8:11], v8, s[26:27]
	s_nop 0
	global_load_dwordx2 v[132:133], v14, s[26:27] offset:16
	global_load_dwordx4 v[128:131], v14, s[26:27]
	v_lshrrev_b32_e32 v14, 16, v15
	v_mad_u32_u24 v14, v14, s21, v110
	global_load_dwordx2 v[138:139], v14, s[26:27] offset:16
	global_load_dwordx4 v[134:137], v14, s[26:27]
	v_and_b32_e32 v14, 0xffff, v16
	v_mad_u32_u24 v14, v14, s21, v110
	ds_read_b128 v[168:171], v95
	ds_read_b128 v[172:175], v95 offset:16
	global_load_dwordx2 v[144:145], v14, s[26:27] offset:16
	global_load_dwordx4 v[140:143], v14, s[26:27]
	v_lshrrev_b32_e32 v15, 16, v16
	v_and_b32_e32 v14, 0xffff, v17
	v_lshrrev_b32_e32 v16, 16, v17
	v_mad_u32_u24 v15, v15, s21, v110
	v_mad_u32_u24 v14, v14, s21, v110
	v_mad_u32_u24 v16, v16, s21, v110
	global_load_dwordx2 v[150:151], v15, s[26:27] offset:16
	global_load_dwordx4 v[146:149], v15, s[26:27]
	global_load_dwordx2 v[156:157], v14, s[26:27] offset:16
	global_load_dwordx4 v[152:155], v14, s[26:27]
	global_load_dwordx2 v[162:163], v16, s[26:27] offset:16
	global_load_dwordx4 v[158:161], v16, s[26:27]
	s_cmpk_gt_i32 s40, 0x7fff
	s_mov_b64 s[34:35], s[24:25]
	s_waitcnt vmcnt(14)
	v_cvt_scalef32_pk32_f16_fp6 v[50:65], v[2:7], 1.0
	s_waitcnt lgkmcnt(1)
	v_pk_fma_f16 v50, v168, v50, 0
	s_waitcnt vmcnt(12)
	v_cvt_scalef32_pk32_f16_fp6 v[34:49], v[8:13], 1.0
	v_pk_fma_f16 v51, v168, v51, 0
	v_pk_fma_f16 v52, v168, v52, 0
	v_pk_fma_f16 v53, v168, v53, 0
	v_pk_fma_f16 v54, v168, v54, 0
	v_pk_fma_f16 v55, v168, v55, 0
	v_pk_fma_f16 v56, v168, v56, 0
	v_pk_fma_f16 v57, v168, v57, 0
	v_pk_fma_f16 v58, v168, v58, 0
	v_pk_fma_f16 v59, v168, v59, 0
	v_pk_fma_f16 v60, v168, v60, 0
	v_pk_fma_f16 v61, v168, v61, 0
	v_pk_fma_f16 v62, v168, v62, 0
	v_pk_fma_f16 v63, v168, v63, 0
	v_pk_fma_f16 v64, v168, v64, 0
	v_pk_fma_f16 v65, v168, v65, 0
	s_waitcnt vmcnt(10)
	v_cvt_scalef32_pk32_f16_fp6 v[18:33], v[128:133], 1.0
	v_pk_fma_f16 v34, v169, v34, v50
	v_pk_fma_f16 v35, v169, v35, v51
	v_pk_fma_f16 v36, v169, v36, v52
	v_pk_fma_f16 v37, v169, v37, v53
	v_pk_fma_f16 v38, v169, v38, v54
	v_pk_fma_f16 v39, v169, v39, v55
	v_pk_fma_f16 v40, v169, v40, v56
	v_pk_fma_f16 v41, v169, v41, v57
	v_pk_fma_f16 v42, v169, v42, v58
	v_pk_fma_f16 v43, v169, v43, v59
	v_pk_fma_f16 v44, v169, v44, v60
	v_pk_fma_f16 v45, v169, v45, v61
	v_pk_fma_f16 v46, v169, v46, v62
	v_pk_fma_f16 v47, v169, v47, v63
	v_pk_fma_f16 v48, v169, v48, v64
	v_pk_fma_f16 v49, v169, v49, v65
	s_waitcnt vmcnt(8)
	v_cvt_scalef32_pk32_f16_fp6 v[2:17], v[134:139], 1.0
	v_pk_fma_f16 v18, v170, v18, v34
	v_pk_fma_f16 v19, v170, v19, v35
	v_pk_fma_f16 v20, v170, v20, v36
	v_pk_fma_f16 v21, v170, v21, v37
	v_pk_fma_f16 v22, v170, v22, v38
	v_pk_fma_f16 v23, v170, v23, v39
	v_pk_fma_f16 v24, v170, v24, v40
	v_pk_fma_f16 v25, v170, v25, v41
	v_pk_fma_f16 v26, v170, v26, v42
	v_pk_fma_f16 v27, v170, v27, v43
	v_pk_fma_f16 v28, v170, v28, v44
	v_pk_fma_f16 v29, v170, v29, v45
	v_pk_fma_f16 v30, v170, v30, v46
	v_pk_fma_f16 v31, v170, v31, v47
	v_pk_fma_f16 v32, v170, v32, v48
	v_pk_fma_f16 v33, v170, v33, v49
	v_pk_fma_f16 v18, v171, v2, v18
	v_pk_fma_f16 v19, v171, v3, v19
	v_pk_fma_f16 v20, v171, v4, v20
	v_pk_fma_f16 v21, v171, v5, v21
	v_pk_fma_f16 v22, v171, v6, v22
	v_pk_fma_f16 v23, v171, v7, v23
	v_pk_fma_f16 v24, v171, v8, v24
	v_pk_fma_f16 v25, v171, v9, v25
	v_pk_fma_f16 v26, v171, v10, v26
	v_pk_fma_f16 v27, v171, v11, v27
	v_pk_fma_f16 v28, v171, v12, v28
	v_pk_fma_f16 v29, v171, v13, v29
	v_pk_fma_f16 v30, v171, v14, v30
	v_pk_fma_f16 v31, v171, v15, v31
	v_pk_fma_f16 v32, v171, v16, v32
	v_pk_fma_f16 v33, v171, v17, v33
	s_waitcnt vmcnt(6)
	v_cvt_scalef32_pk32_f16_fp6 v[2:17], v[140:145], 1.0
	s_waitcnt lgkmcnt(0)
	v_pk_fma_f16 v18, v172, v2, v18
	v_pk_fma_f16 v34, v172, v3, v19
	v_pk_fma_f16 v35, v172, v4, v20
	v_pk_fma_f16 v36, v172, v5, v21
	v_pk_fma_f16 v37, v172, v6, v22
	v_pk_fma_f16 v38, v172, v7, v23
	v_pk_fma_f16 v24, v172, v8, v24
	v_pk_fma_f16 v25, v172, v9, v25
	v_pk_fma_f16 v26, v172, v10, v26
	v_pk_fma_f16 v27, v172, v11, v27
	v_pk_fma_f16 v28, v172, v12, v28
	v_pk_fma_f16 v29, v172, v13, v29
	v_pk_fma_f16 v30, v172, v14, v30
	v_pk_fma_f16 v31, v172, v15, v31
	v_pk_fma_f16 v32, v172, v16, v32
	v_pk_fma_f16 v33, v172, v17, v33
	s_waitcnt vmcnt(4)
	v_cvt_scalef32_pk32_f16_fp6 v[2:17], v[146:151], 1.0
	v_pk_fma_f16 v39, v173, v2, v18
	v_and_b32_e32 v2, 0xffff, v164
	v_mad_u32_u24 v2, v2, s21, v110
	global_load_dwordx2 v[22:23], v2, s[26:27] offset:16
	global_load_dwordx4 v[18:21], v2, s[26:27]
	v_lshrrev_b32_e32 v2, 16, v164
	v_mad_u32_u24 v2, v2, s21, v110
	v_pk_fma_f16 v34, v173, v3, v34
	v_pk_fma_f16 v35, v173, v4, v35
	v_pk_fma_f16 v36, v173, v5, v36
	v_pk_fma_f16 v37, v173, v6, v37
	v_pk_fma_f16 v38, v173, v7, v38
	v_pk_fma_f16 v40, v173, v8, v24
	v_pk_fma_f16 v41, v173, v9, v25
	v_pk_fma_f16 v42, v173, v10, v26
	v_pk_fma_f16 v43, v173, v11, v27
	v_pk_fma_f16 v44, v173, v12, v28
	v_pk_fma_f16 v45, v173, v13, v29
	v_pk_fma_f16 v46, v173, v14, v30
	v_pk_fma_f16 v47, v173, v15, v31
	global_load_dwordx2 v[28:29], v2, s[26:27] offset:16
	global_load_dwordx4 v[24:27], v2, s[26:27]
	v_pk_fma_f16 v48, v173, v16, v32
	v_pk_fma_f16 v49, v173, v17, v33
	s_waitcnt vmcnt(6)
	v_cvt_scalef32_pk32_f16_fp6 v[2:17], v[152:157], 1.0
	v_pk_fma_f16 v39, v174, v2, v39
	v_and_b32_e32 v2, 0xffff, v165
	v_mad_u32_u24 v2, v2, s21, v110
	v_pk_fma_f16 v50, v174, v3, v34
	v_pk_fma_f16 v51, v174, v4, v35
	v_pk_fma_f16 v36, v174, v5, v36
	v_pk_fma_f16 v37, v174, v6, v37
	v_pk_fma_f16 v38, v174, v7, v38
	v_pk_fma_f16 v52, v174, v8, v40
	v_pk_fma_f16 v53, v174, v9, v41
	v_pk_fma_f16 v42, v174, v10, v42
	v_pk_fma_f16 v43, v174, v11, v43
	global_load_dwordx2 v[34:35], v2, s[26:27] offset:16
	global_load_dwordx4 v[30:33], v2, s[26:27]
	v_pk_fma_f16 v44, v174, v12, v44
	v_pk_fma_f16 v45, v174, v13, v45
	v_pk_fma_f16 v46, v174, v14, v46
	v_pk_fma_f16 v47, v174, v15, v47
	v_pk_fma_f16 v48, v174, v16, v48
	v_pk_fma_f16 v49, v174, v17, v49
	s_waitcnt vmcnt(6)
	v_cvt_scalef32_pk32_f16_fp6 v[2:17], v[158:163], 1.0
	v_pk_fma_f16 v127, v175, v2, v39
	v_lshrrev_b32_e32 v2, 16, v165
	v_mad_u32_u24 v2, v2, s21, v110
	v_pk_fma_f16 v138, v175, v5, v36
	v_pk_fma_f16 v139, v175, v6, v37
	v_pk_fma_f16 v140, v175, v7, v38
	global_load_dwordx2 v[40:41], v2, s[26:27] offset:16
	global_load_dwordx4 v[36:39], v2, s[26:27]
	v_and_b32_e32 v2, 0xffff, v166
	v_mad_u32_u24 v2, v2, s21, v110
	v_pk_fma_f16 v143, v175, v10, v42
	v_pk_fma_f16 v144, v175, v11, v43
	v_pk_fma_f16 v145, v175, v12, v44
	v_pk_fma_f16 v146, v175, v13, v45
	v_pk_fma_f16 v147, v175, v14, v46
	v_pk_fma_f16 v148, v175, v15, v47
	ds_read_b128 v[128:131], v95 offset:256
	ds_read_b128 v[132:135], v95 offset:272
	global_load_dwordx2 v[46:47], v2, s[26:27] offset:16
	global_load_dwordx4 v[42:45], v2, s[26:27]
	v_lshrrev_b32_e32 v2, 16, v166
	v_mad_u32_u24 v2, v2, s21, v110
	v_pk_fma_f16 v136, v175, v3, v50
	v_pk_fma_f16 v137, v175, v4, v51
	v_pk_fma_f16 v141, v175, v8, v52
	v_pk_fma_f16 v142, v175, v9, v53
	v_pk_fma_f16 v149, v175, v16, v48
	v_pk_fma_f16 v150, v175, v17, v49
	global_load_dwordx2 v[52:53], v2, s[26:27] offset:16
	global_load_dwordx4 v[48:51], v2, s[26:27]
	v_and_b32_e32 v2, 0xffff, v167
	v_mad_u32_u24 v2, v2, s21, v110
	global_load_dwordx2 v[58:59], v2, s[26:27] offset:16
	global_load_dwordx4 v[54:57], v2, s[26:27]
	v_lshrrev_b32_e32 v2, 16, v167
	v_mad_u32_u24 v2, v2, s21, v110
	global_load_dwordx2 v[64:65], v2, s[26:27] offset:16
	global_load_dwordx4 v[60:63], v2, s[26:27]
	s_waitcnt vmcnt(14)
	v_cvt_scalef32_pk32_f16_fp6 v[2:17], v[18:23], 1.0
	s_waitcnt lgkmcnt(1)
	v_pk_fma_f16 v18, v128, v2, v127
	v_pk_fma_f16 v19, v128, v3, v136
	v_pk_fma_f16 v20, v128, v4, v137
	v_pk_fma_f16 v21, v128, v5, v138
	v_pk_fma_f16 v22, v128, v6, v139
	v_pk_fma_f16 v23, v128, v7, v140
	v_pk_fma_f16 v95, v128, v8, v141
	v_pk_fma_f16 v127, v128, v9, v142
	v_pk_fma_f16 v136, v128, v10, v143
	v_pk_fma_f16 v137, v128, v11, v144
	v_pk_fma_f16 v138, v128, v12, v145
	v_pk_fma_f16 v139, v128, v13, v146
	v_pk_fma_f16 v140, v128, v14, v147
	v_pk_fma_f16 v141, v128, v15, v148
	v_pk_fma_f16 v142, v128, v16, v149
	v_pk_fma_f16 v128, v128, v17, v150
	s_waitcnt vmcnt(12)
	v_cvt_scalef32_pk32_f16_fp6 v[2:17], v[24:29], 1.0
	v_pk_fma_f16 v18, v129, v2, v18
	v_pk_fma_f16 v19, v129, v3, v19
	v_pk_fma_f16 v20, v129, v4, v20
	v_pk_fma_f16 v21, v129, v5, v21
	v_pk_fma_f16 v22, v129, v6, v22
	v_pk_fma_f16 v23, v129, v7, v23
	v_pk_fma_f16 v24, v129, v8, v95
	v_pk_fma_f16 v25, v129, v9, v127
	v_pk_fma_f16 v26, v129, v10, v136
	v_pk_fma_f16 v27, v129, v11, v137
	v_pk_fma_f16 v28, v129, v12, v138
	v_pk_fma_f16 v29, v129, v13, v139
	v_pk_fma_f16 v95, v129, v14, v140
	v_pk_fma_f16 v127, v129, v15, v141
	v_pk_fma_f16 v136, v129, v16, v142
	v_pk_fma_f16 v128, v129, v17, v128
	s_waitcnt vmcnt(10)
	v_cvt_scalef32_pk32_f16_fp6 v[2:17], v[30:35], 1.0
	v_pk_fma_f16 v18, v130, v2, v18
	v_pk_fma_f16 v19, v130, v3, v19
	v_pk_fma_f16 v20, v130, v4, v20
	v_pk_fma_f16 v21, v130, v5, v21
	v_pk_fma_f16 v22, v130, v6, v22
	v_pk_fma_f16 v23, v130, v7, v23
	v_pk_fma_f16 v24, v130, v8, v24
	v_pk_fma_f16 v25, v130, v9, v25
	v_pk_fma_f16 v26, v130, v10, v26
	v_pk_fma_f16 v27, v130, v11, v27
	v_pk_fma_f16 v28, v130, v12, v28
	v_pk_fma_f16 v29, v130, v13, v29
	v_pk_fma_f16 v30, v130, v14, v95
	v_pk_fma_f16 v31, v130, v15, v127
	v_pk_fma_f16 v32, v130, v16, v136
	v_pk_fma_f16 v33, v130, v17, v128
	s_waitcnt vmcnt(8)
	v_cvt_scalef32_pk32_f16_fp6 v[2:17], v[36:41], 1.0
	v_pk_fma_f16 v18, v131, v2, v18
	v_pk_fma_f16 v19, v131, v3, v19
	v_pk_fma_f16 v20, v131, v4, v20
	v_pk_fma_f16 v21, v131, v5, v21
	v_pk_fma_f16 v22, v131, v6, v22
	v_pk_fma_f16 v23, v131, v7, v23
	v_pk_fma_f16 v24, v131, v8, v24
	v_pk_fma_f16 v25, v131, v9, v25
	v_pk_fma_f16 v26, v131, v10, v26
	v_pk_fma_f16 v27, v131, v11, v27
	v_pk_fma_f16 v28, v131, v12, v28
	v_pk_fma_f16 v29, v131, v13, v29
	v_pk_fma_f16 v30, v131, v14, v30
	v_pk_fma_f16 v31, v131, v15, v31
	v_pk_fma_f16 v32, v131, v16, v32
	v_pk_fma_f16 v33, v131, v17, v33
	s_waitcnt vmcnt(6)
	v_cvt_scalef32_pk32_f16_fp6 v[2:17], v[42:47], 1.0
	s_waitcnt lgkmcnt(0)
	v_pk_fma_f16 v18, v132, v2, v18
	v_pk_fma_f16 v19, v132, v3, v19
	v_pk_fma_f16 v20, v132, v4, v20
	v_pk_fma_f16 v21, v132, v5, v21
	v_pk_fma_f16 v22, v132, v6, v22
	v_pk_fma_f16 v23, v132, v7, v23
	v_pk_fma_f16 v24, v132, v8, v24
	v_pk_fma_f16 v25, v132, v9, v25
	v_pk_fma_f16 v26, v132, v10, v26
	v_pk_fma_f16 v27, v132, v11, v27
	v_pk_fma_f16 v28, v132, v12, v28
	v_pk_fma_f16 v29, v132, v13, v29
	v_pk_fma_f16 v30, v132, v14, v30
	v_pk_fma_f16 v31, v132, v15, v31
	v_pk_fma_f16 v32, v132, v16, v32
	v_pk_fma_f16 v33, v132, v17, v33
	s_waitcnt vmcnt(4)
	v_cvt_scalef32_pk32_f16_fp6 v[2:17], v[48:53], 1.0
	v_pk_fma_f16 v18, v133, v2, v18
	v_pk_fma_f16 v19, v133, v3, v19
	v_pk_fma_f16 v20, v133, v4, v20
	v_pk_fma_f16 v21, v133, v5, v21
	v_pk_fma_f16 v22, v133, v6, v22
	v_pk_fma_f16 v23, v133, v7, v23
	v_pk_fma_f16 v24, v133, v8, v24
	v_pk_fma_f16 v25, v133, v9, v25
	v_pk_fma_f16 v26, v133, v10, v26
	v_pk_fma_f16 v27, v133, v11, v27
	v_pk_fma_f16 v28, v133, v12, v28
	v_pk_fma_f16 v29, v133, v13, v29
	v_pk_fma_f16 v30, v133, v14, v30
	v_pk_fma_f16 v31, v133, v15, v31
	v_pk_fma_f16 v32, v133, v16, v32
	v_pk_fma_f16 v33, v133, v17, v33
	s_waitcnt vmcnt(2)
	v_cvt_scalef32_pk32_f16_fp6 v[2:17], v[54:59], 1.0
	v_pk_fma_f16 v18, v134, v2, v18
	v_pk_fma_f16 v19, v134, v3, v19
	v_pk_fma_f16 v20, v134, v4, v20
	v_pk_fma_f16 v21, v134, v5, v21
	v_pk_fma_f16 v22, v134, v6, v22
	v_pk_fma_f16 v23, v134, v7, v23
	v_pk_fma_f16 v24, v134, v8, v24
	v_pk_fma_f16 v25, v134, v9, v25
	v_pk_fma_f16 v26, v134, v10, v26
	v_pk_fma_f16 v27, v134, v11, v27
	v_pk_fma_f16 v28, v134, v12, v28
	v_pk_fma_f16 v29, v134, v13, v29
	v_pk_fma_f16 v30, v134, v14, v30
	v_pk_fma_f16 v31, v134, v15, v31
	v_pk_fma_f16 v32, v134, v16, v32
	v_pk_fma_f16 v33, v134, v17, v33
	s_waitcnt vmcnt(0)
	v_cvt_scalef32_pk32_f16_fp6 v[2:17], v[60:65], 1.0
	v_pk_fma_f16 v2, v135, v2, v18
	v_pk_fma_f16 v4, v135, v4, v20
	v_pk_fma_f16 v6, v135, v6, v22
	v_pk_fma_f16 v8, v135, v8, v24
	v_pk_fma_f16 v10, v135, v10, v26
	v_pk_fma_f16 v12, v135, v12, v28
	v_pk_fma_f16 v14, v135, v14, v30
	v_pk_fma_f16 v16, v135, v16, v32
	v_pk_fma_f16 v3, v135, v3, v19
	v_pk_fma_f16 v5, v135, v5, v21
	v_pk_fma_f16 v7, v135, v7, v23
	v_pk_fma_f16 v9, v135, v9, v25
	v_pk_fma_f16 v11, v135, v11, v27
	v_pk_fma_f16 v13, v135, v13, v29
	v_pk_fma_f16 v15, v135, v15, v31
	v_pk_fma_f16 v17, v135, v17, v33
	v_permlane32_swap_b32_e32 v2, v10
	v_permlane32_swap_b32_e32 v4, v12
	v_permlane32_swap_b32_e32 v6, v14
	v_permlane32_swap_b32_e32 v8, v16
	v_pk_add_f16 v2, v2, v10
	v_permlane32_swap_b32_e32 v3, v11
	v_pk_add_f16 v4, v4, v12
	v_permlane32_swap_b32_e32 v5, v13
	v_pk_add_f16 v6, v6, v14
	v_permlane32_swap_b32_e32 v7, v15
	v_pk_add_f16 v8, v8, v16
	v_permlane32_swap_b32_e32 v9, v17
	v_pk_add_f16 v3, v3, v11
	v_pk_add_f16 v5, v5, v13
	v_pk_add_f16 v7, v7, v15
	v_pk_add_f16 v9, v9, v17
	v_permlane16_swap_b32_e32 v2, v6
	v_permlane16_swap_b32_e32 v4, v8
	v_pk_add_f16 v2, v2, v6
	v_permlane16_swap_b32_e32 v3, v7
	v_pk_add_f16 v4, v4, v8
	v_permlane16_swap_b32_e32 v5, v9
	v_pk_add_f16 v3, v3, v7
	v_pk_add_f16 v5, v5, v9
	v_cndmask_b32_e64 v7, v2, v4, s[4:5]
	v_mov_b32_e32 v6, 0
	v_cndmask_b32_e64 v8, v3, v5, s[4:5]
	s_nop 0
	v_mov_b32_dpp v6, v7 row_ror:8 row_mask:0xf bank_mask:0xf
	v_mov_b32_e32 v7, 0
	s_nop 1
	v_mov_b32_dpp v7, v8 row_ror:8 row_mask:0xf bank_mask:0xf
	s_cbranch_scc1 .LBB0_758
	s_ashr_i32 s34, s40, 11
	s_mul_hi_i32 s35, s34, 0xc000
	s_mul_i32 s34, s34, 0xc000
	s_add_u32 s34, s3, s34
	s_addc_u32 s35, s59, s35

.LBB0_1294:
	s_cmpk_gt_i32 s90, 0x3fff
	s_cbranch_scc1 .LBB0_1303
	s_waitcnt vmcnt(0)
	v_mbcnt_hi_u32_b32 v2, -1, v208
	v_and_b32_e32 v3, 64, v2
	v_add_u32_e32 v3, 64, v3
	v_xor_b32_e32 v4, 1, v2
	v_cmp_lt_i32_e32 vcc, v4, v3
	s_lshl_b32 s0, s89, 13
	s_ashr_i32 s91, s90, 31
	v_cndmask_b32_e32 v4, v2, v4, vcc
	v_lshlrev_b32_e32 v44, 2, v4
	v_xor_b32_e32 v4, 2, v2
	v_cmp_lt_i32_e32 vcc, v4, v3
	s_add_i32 s16, s0, 0
	s_lshl_b64 s[12:13], s[90:91], 2
	v_cndmask_b32_e32 v4, v2, v4, vcc
	v_lshlrev_b32_e32 v45, 2, v4
	v_xor_b32_e32 v4, 4, v2
	v_cmp_lt_i32_e32 vcc, v4, v3
	s_add_u32 s2, s82, s12
	s_addc_u32 s3, s83, s13
	v_cndmask_b32_e32 v4, v2, v4, vcc
	v_lshlrev_b32_e32 v46, 2, v4
	v_xor_b32_e32 v4, 8, v2
	v_cmp_lt_i32_e32 vcc, v4, v3
	s_add_u32 s14, s2, 0x300000
	s_addc_u32 s15, s3, 0
	v_cndmask_b32_e32 v4, v2, v4, vcc
	v_lshlrev_b32_e32 v47, 2, v4
	v_xor_b32_e32 v4, 16, v2
	v_cmp_lt_i32_e32 vcc, v4, v3
	s_lshl_b64 s[2:3], s[90:91], 13
	v_mul_u32_u24_e32 v34, 24, v206
	v_cndmask_b32_e32 v4, v2, v4, vcc
	v_lshlrev_b32_e32 v48, 2, v4
	v_xor_b32_e32 v4, 32, v2
	v_cmp_lt_i32_e32 vcc, v4, v3
	v_mov_b32_e32 v3, s3
	v_mov_b32_e32 v35, 0
	v_cndmask_b32_e32 v2, v2, v4, vcc
	v_lshlrev_b32_e32 v49, 2, v2
	v_lshl_or_b32 v2, v204, 4, s2
	s_mov_b64 s[2:3], 0x8000000
	v_lshl_add_u64 v[36:37], v[2:3], 0, s[2:3]
	s_mul_hi_i32 s2, s90, 0xc0
	s_mul_i32 s3, s90, 0xc0
	v_mov_b32_e32 v2, s3
	v_mov_b32_e32 v3, s2
	s_mov_b32 s2, 0x300000
	v_mad_u64_u32 v[2:3], s[2:3], v1, s2, v[2:3]
	v_readlane_b32 s36, v254, 2
	v_lshl_add_u64 v[2:3], v[2:3], 0, v[34:35]
	v_lshlrev_b32_e32 v4, 4, v204
	v_lshlrev_b32_e32 v5, 7, v204
	s_ashr_i32 s87, s86, 31
	v_readlane_b32 s50, v254, 16
	v_readlane_b32 s51, v254, 17
	v_lshl_add_u64 v[40:41], s[82:83], 0, v[2:3]
	s_mov_b64 s[2:3], 0x5400008
	v_cmp_eq_u32_e64 s[0:1], 0, v204
	s_lshl_b64 s[6:7], s[86:87], 2
	v_lshl_add_u64 v[38:39], s[50:51], 0, v[36:37]
	s_lshl_b64 s[8:9], s[86:87], 13
	v_lshl_add_u64 v[42:43], v[40:41], 0, s[2:3]
	s_mul_hi_i32 s11, s86, 0xc0
	s_mul_i32 s10, s86, 0xc0
	s_movk_i32 s2, 0x1000
	s_mov_b32 s3, 0xda24260
	s_mov_b32 s18, 0x40e00000
	s_mov_b32 s19, 0x800000
	v_mov_b32_e32 v52, 0x42000000
	s_mov_b32 s20, 0xc2fc0000
	v_mov_b32_e32 v53, 0x42800000
	v_not_b32_e32 v54, 63
	v_add_u32_e32 v50, s16, v4
	v_add_u32_e32 v51, s16, v5
	s_mov_b32 s21, s90
	v_readlane_b32 s37, v254, 3
	v_readlane_b32 s38, v254, 4
	v_readlane_b32 s39, v254, 5
	v_readlane_b32 s40, v254, 6
	v_readlane_b32 s41, v254, 7
	v_readlane_b32 s42, v254, 8
	v_readlane_b32 s43, v254, 9
	v_readlane_b32 s44, v254, 10
	v_readlane_b32 s45, v254, 11
	v_readlane_b32 s46, v254, 12
	v_readlane_b32 s47, v254, 13
	v_readlane_b32 s48, v254, 14
	v_readlane_b32 s49, v254, 15
	s_branch .LBB0_1297

.LBB0_1297:
	global_load_dwordx4 v[2:5], v[38:39], off
	global_load_dwordx4 v[6:9], v[38:39], off offset:1024
	global_load_dwordx4 v[10:13], v[38:39], off offset:2048
	global_load_dwordx4 v[14:17], v[38:39], off offset:3072
	v_add_co_u32_e32 v56, vcc, s2, v38
	s_waitcnt vmcnt(0)
	v_max_f32_e64 v34, |v5|, |v5|
	v_addc_co_u32_e32 v57, vcc, 0, v39, vcc
	global_load_dwordx4 v[18:21], v[56:57], off
	global_load_dwordx4 v[22:25], v[56:57], off offset:1024
	global_load_dwordx4 v[26:29], v[56:57], off offset:2048
	global_load_dwordx4 v[30:33], v[56:57], off offset:3072
	v_max_f32_e64 v55, |v4|, |v4|
	v_max_f32_e64 v56, |v9|, |v9|
	v_max_f32_e64 v57, |v8|, |v8|
	v_max_f32_e64 v58, |v13|, |v13|
	v_max_f32_e64 v59, |v12|, |v12|
	v_max_f32_e64 v60, |v17|, |v17|
	v_max_f32_e64 v61, |v16|, |v16|
	v_max_f32_e32 v34, v55, v34
	v_max_f32_e32 v55, v57, v56
	v_max_f32_e32 v56, v59, v58
	v_max_f32_e32 v57, v61, v60
	v_max3_f32 v34, |v2|, |v3|, v34
	v_max3_f32 v55, |v6|, |v7|, v55
	v_max3_f32 v56, |v10|, |v11|, v56
	v_max3_f32 v57, |v14|, |v15|, v57
	v_max3_f32 v34, v34, 0, v55
	v_max3_f32 v34, v34, v56, v57
	s_waitcnt vmcnt(0)
	v_max_f32_e64 v58, |v21|, |v21|
	v_max_f32_e64 v59, |v20|, |v20|
	v_max_f32_e64 v60, |v25|, |v25|
	v_max_f32_e64 v61, |v24|, |v24|
	v_max_f32_e64 v62, |v29|, |v29|
	v_max_f32_e64 v63, |v28|, |v28|
	v_max_f32_e64 v64, |v33|, |v33|
	v_max_f32_e64 v65, |v32|, |v32|
	v_max_f32_e32 v58, v59, v58
	v_max_f32_e32 v59, v61, v60
	v_max_f32_e32 v60, v63, v62
	v_max_f32_e32 v61, v65, v64
	v_max3_f32 v55, |v18|, |v19|, v58
	v_max3_f32 v58, |v22|, |v23|, v59
	v_max3_f32 v59, |v26|, |v27|, v60
	v_max3_f32 v60, |v30|, |v31|, v61
	v_max3_f32 v34, v34, v55, v58
	v_max3_f32 v34, v34, v59, v60
	ds_bpermute_b32 v55, v44, v34
	s_waitcnt lgkmcnt(0)
	v_max_f32_e32 v55, v55, v55
	v_max_f32_e32 v34, v34, v55
	ds_bpermute_b32 v55, v45, v34
	s_waitcnt lgkmcnt(0)
	v_max_f32_e32 v55, v55, v55
	v_max_f32_e32 v34, v34, v55
	ds_bpermute_b32 v55, v46, v34
	s_waitcnt lgkmcnt(0)
	v_max_f32_e32 v55, v55, v55
	v_max_f32_e32 v34, v34, v55
	ds_bpermute_b32 v55, v47, v34
	s_waitcnt lgkmcnt(0)
	v_max_f32_e32 v55, v55, v55
	v_max_f32_e32 v34, v34, v55
	ds_bpermute_b32 v55, v48, v34
	s_waitcnt lgkmcnt(0)
	v_max_f32_e32 v55, v55, v55
	v_max_f32_e32 v34, v34, v55
	ds_bpermute_b32 v55, v49, v34
	s_waitcnt lgkmcnt(0)
	v_max3_f32 v34, v34, v55, s3
	v_div_scale_f32 v55, s[16:17], v34, v34, s18
	v_rcp_f32_e32 v56, v55
	v_div_scale_f32 v57, vcc, s18, v34, s18
	v_fma_f32 v58, -v55, v56, 1.0
	v_fmac_f32_e32 v56, v58, v56
	v_mul_f32_e32 v58, v57, v56
	v_fma_f32 v59, -v55, v58, v57
	v_fmac_f32_e32 v58, v59, v56
	v_fma_f32 v55, -v55, v58, v57
	v_div_fmas_f32 v55, v55, v56, v58
	v_div_fixup_f32 v34, v55, v34, s18
	v_cmp_gt_f32_e32 vcc, s19, v34
	s_nop 1
	v_cndmask_b32_e64 v55, 0, 32, vcc
	v_ldexp_f32 v34, v34, v55
	v_log_f32_e32 v34, v34
	v_cndmask_b32_e32 v55, 0, v52, vcc
	v_sub_f32_e32 v34, v34, v55
	v_floor_f32_e32 v34, v34
	v_cmp_gt_f32_e32 vcc, s20, v34
	s_nop 1
	v_cndmask_b32_e32 v55, 0, v53, vcc
	v_add_f32_e32 v34, v34, v55
	v_exp_f32_e32 v34, v34
	v_cndmask_b32_e32 v55, 0, v54, vcc
	v_ldexp_f32 v34, v34, v55
	v_pk_mul_f32 v[4:5], v[4:5], v[34:35] op_sel_hi:[1,0]
	v_pk_mul_f32 v[2:3], v[2:3], v[34:35] op_sel_hi:[1,0]
	v_pk_mul_f32 v[8:9], v[8:9], v[34:35] op_sel_hi:[1,0]
	v_pk_mul_f32 v[6:7], v[6:7], v[34:35] op_sel_hi:[1,0]
	v_pk_mul_f32 v[12:13], v[12:13], v[34:35] op_sel_hi:[1,0]
	v_pk_mul_f32 v[10:11], v[10:11], v[34:35] op_sel_hi:[1,0]
	v_pk_mul_f32 v[16:17], v[16:17], v[34:35] op_sel_hi:[1,0]
	v_pk_mul_f32 v[14:15], v[14:15], v[34:35] op_sel_hi:[1,0]
	v_pk_mul_f32 v[20:21], v[20:21], v[34:35] op_sel_hi:[1,0]
	v_pk_mul_f32 v[18:19], v[18:19], v[34:35] op_sel_hi:[1,0]
	v_pk_mul_f32 v[24:25], v[24:25], v[34:35] op_sel_hi:[1,0]
	v_pk_mul_f32 v[22:23], v[22:23], v[34:35] op_sel_hi:[1,0]
	v_pk_mul_f32 v[28:29], v[28:29], v[34:35] op_sel_hi:[1,0]
	v_pk_mul_f32 v[26:27], v[26:27], v[34:35] op_sel_hi:[1,0]
	v_pk_mul_f32 v[32:33], v[32:33], v[34:35] op_sel_hi:[1,0]
	v_pk_mul_f32 v[30:31], v[30:31], v[34:35] op_sel_hi:[1,0]
	ds_write_b128 v50, v[2:5]
	ds_write_b128 v50, v[6:9] offset:1024
	ds_write_b128 v50, v[10:13] offset:2048
	ds_write_b128 v50, v[14:17] offset:3072
	ds_write_b128 v50, v[18:21] offset:4096
	ds_write_b128 v50, v[22:25] offset:5120
	ds_write_b128 v50, v[26:29] offset:6144
	ds_write_b128 v50, v[30:33] offset:7168
	s_waitcnt lgkmcnt(0)
	ds_read_b128 v[18:21], v51
	ds_read_b128 v[22:25], v51 offset:16
	ds_read_b128 v[26:29], v51 offset:32
	ds_read_b128 v[30:33], v51 offset:48
	ds_read_b128 v[56:59], v51 offset:64
	ds_read_b128 v[60:63], v51 offset:80
	ds_read_b128 v[64:67], v51 offset:96
	ds_read_b128 v[68:71], v51 offset:112
	s_waitcnt lgkmcnt(7)
	v_mov_b32_e32 v2, v18
	v_mov_b32_e32 v3, v20
	s_waitcnt lgkmcnt(6)
	v_mov_b32_e32 v4, v22
	v_mov_b32_e32 v5, v24
	s_waitcnt lgkmcnt(5)
	v_mov_b32_e32 v6, v26
	v_mov_b32_e32 v7, v28
	s_waitcnt lgkmcnt(4)
	v_mov_b32_e32 v8, v30
	v_mov_b32_e32 v9, v32
	s_waitcnt lgkmcnt(3)
	v_mov_b32_e32 v10, v56
	v_mov_b32_e32 v11, v58
	s_waitcnt lgkmcnt(2)
	v_mov_b32_e32 v12, v60
	v_mov_b32_e32 v13, v62
	s_waitcnt lgkmcnt(1)
	v_mov_b32_e32 v14, v64
	v_mov_b32_e32 v15, v66
	s_waitcnt lgkmcnt(0)
	v_mov_b32_e32 v16, v68
	v_mov_b32_e32 v17, v70
	v_mov_b32_e32 v18, v19
	v_mov_b32_e32 v19, v21
	v_mov_b32_e32 v20, v23
	v_mov_b32_e32 v21, v25
	v_mov_b32_e32 v22, v27
	v_mov_b32_e32 v23, v29
	v_mov_b32_e32 v24, v31
	v_mov_b32_e32 v25, v33
	v_mov_b32_e32 v26, v57
	v_mov_b32_e32 v27, v59
	v_mov_b32_e32 v28, v61
	v_mov_b32_e32 v29, v63
	v_mov_b32_e32 v30, v65
	v_mov_b32_e32 v31, v67
	v_mov_b32_e32 v32, v69
	v_mov_b32_e32 v33, v71
	v_cvt_scalef32_2xpk16_fp6_f32 v[2:7], v[2:17], v[18:33], 1.0
	global_store_dwordx4 v[42:43], v[2:5], off offset:-8
	global_store_dwordx2 v[42:43], v[6:7], off offset:8
	s_and_saveexec_b64 s[16:17], s[0:1]
	s_cbranch_execz .LBB0_1296
	v_div_scale_f32 v2, s[22:23], v34, v34, 1.0
	v_rcp_f32_e32 v3, v2
	v_div_scale_f32 v4, vcc, 1.0, v34, 1.0
	v_fma_f32 v5, -v2, v3, 1.0
	v_fmac_f32_e32 v3, v5, v3
	v_mul_f32_e32 v5, v4, v3
	v_fma_f32 v6, -v2, v5, v4
	v_fmac_f32_e32 v5, v6, v3
	v_fma_f32 v2, -v2, v5, v4
	v_div_fmas_f32 v2, v2, v3, v5
	v_div_fixup_f32 v2, v2, v34, 1.0
	global_store_dword v35, v2, s[14:15]
	s_branch .LBB0_1296

.LBB0_1301:
	global_load_dwordx4 v[2:5], v[34:35], off
	global_load_dwordx4 v[6:9], v[34:35], off offset:1024
	global_load_dwordx4 v[10:13], v[34:35], off offset:2048
	global_load_dwordx4 v[14:17], v[34:35], off offset:3072
	v_add_co_u32_e32 v52, vcc, s2, v34
	s_waitcnt vmcnt(3)
	v_max_f32_e64 v38, |v5|, |v5|
	v_addc_co_u32_e32 v53, vcc, 0, v35, vcc
	global_load_dwordx4 v[18:21], v[52:53], off
	global_load_dwordx4 v[22:25], v[52:53], off offset:1024
	global_load_dwordx4 v[26:29], v[52:53], off offset:2048
	global_load_dwordx4 v[30:33], v[52:53], off offset:3072
	v_max_f32_e64 v43, |v4|, |v4|
	s_waitcnt vmcnt(6)
	v_max_f32_e64 v52, |v9|, |v9|
	v_max_f32_e64 v53, |v8|, |v8|
	s_waitcnt vmcnt(5)
	v_max_f32_e64 v54, |v13|, |v13|
	v_max_f32_e64 v55, |v12|, |v12|
	s_waitcnt vmcnt(4)
	v_max_f32_e64 v56, |v17|, |v17|
	v_max_f32_e64 v57, |v16|, |v16|
	v_max_f32_e32 v38, v43, v38
	v_max_f32_e32 v43, v53, v52
	v_max_f32_e32 v52, v55, v54
	v_max_f32_e32 v53, v57, v56
	v_max3_f32 v38, |v2|, |v3|, v38
	v_max3_f32 v43, |v6|, |v7|, v43
	v_max3_f32 v52, |v10|, |v11|, v52
	v_max3_f32 v53, |v14|, |v15|, v53
	v_max3_f32 v38, v38, 0, v43
	v_max3_f32 v38, v38, v52, v53
	s_waitcnt vmcnt(3)
	v_max_f32_e64 v54, |v21|, |v21|
	v_max_f32_e64 v55, |v20|, |v20|
	s_waitcnt vmcnt(2)
	v_max_f32_e64 v56, |v25|, |v25|
	v_max_f32_e64 v57, |v24|, |v24|
	s_waitcnt vmcnt(1)
	v_max_f32_e64 v58, |v29|, |v29|
	v_max_f32_e64 v59, |v28|, |v28|
	s_waitcnt vmcnt(0)
	v_max_f32_e64 v60, |v33|, |v33|
	v_max_f32_e64 v61, |v32|, |v32|
	v_max_f32_e32 v54, v55, v54
	v_max_f32_e32 v55, v57, v56
	v_max_f32_e32 v56, v59, v58
	v_max_f32_e32 v57, v61, v60
	v_max3_f32 v43, |v18|, |v19|, v54
	v_max3_f32 v54, |v22|, |v23|, v55
	v_max3_f32 v55, |v26|, |v27|, v56
	v_max3_f32 v56, |v30|, |v31|, v57
	v_max3_f32 v38, v38, v43, v54
	v_max3_f32 v38, v38, v55, v56
	ds_bpermute_b32 v43, v44, v38
	s_waitcnt lgkmcnt(0)
	v_max_f32_e32 v43, v43, v43
	v_max_f32_e32 v38, v38, v43
	ds_bpermute_b32 v43, v45, v38
	s_waitcnt lgkmcnt(0)
	v_max_f32_e32 v43, v43, v43
	v_max_f32_e32 v38, v38, v43
	ds_bpermute_b32 v43, v46, v38
	s_waitcnt lgkmcnt(0)
	v_max_f32_e32 v43, v43, v43
	v_max_f32_e32 v38, v38, v43
	ds_bpermute_b32 v43, v47, v38
	s_waitcnt lgkmcnt(0)
	v_max_f32_e32 v43, v43, v43
	v_max_f32_e32 v38, v38, v43
	ds_bpermute_b32 v43, v48, v38
	s_waitcnt lgkmcnt(0)
	v_max_f32_e32 v43, v43, v43
	v_max_f32_e32 v38, v38, v43
	ds_bpermute_b32 v43, v49, v38
	s_waitcnt lgkmcnt(0)
	v_max3_f32 v38, v38, v43, s3
	v_div_scale_f32 v43, s[14:15], v38, v38, s16
	v_rcp_f32_e32 v52, v43
	v_div_scale_f32 v53, vcc, s16, v38, s16
	v_fma_f32 v54, -v43, v52, 1.0
	v_fmac_f32_e32 v52, v54, v52
	v_mul_f32_e32 v54, v53, v52
	v_fma_f32 v55, -v43, v54, v53
	v_fmac_f32_e32 v54, v55, v52
	v_fma_f32 v43, -v43, v54, v53
	v_div_fmas_f32 v43, v43, v52, v54
	v_div_fixup_f32 v38, v43, v38, s16
	v_cmp_gt_f32_e32 vcc, s17, v38
	s_nop 1
	v_cndmask_b32_e64 v43, 0, 32, vcc
	v_ldexp_f32 v38, v38, v43
	v_log_f32_e32 v38, v38
	v_cndmask_b32_e32 v43, 0, v39, vcc
	v_sub_f32_e32 v38, v38, v43
	v_floor_f32_e32 v38, v38
	v_cmp_gt_f32_e32 vcc, s18, v38
	s_nop 1
	v_cndmask_b32_e32 v43, 0, v40, vcc
	v_add_f32_e32 v38, v38, v43
	v_exp_f32_e32 v38, v38
	v_cndmask_b32_e32 v43, 0, v41, vcc
	v_ldexp_f32 v38, v38, v43
	v_pk_mul_f32 v[4:5], v[4:5], v[38:39] op_sel_hi:[1,0]
	v_pk_mul_f32 v[2:3], v[2:3], v[38:39] op_sel_hi:[1,0]
	v_pk_mul_f32 v[8:9], v[8:9], v[38:39] op_sel_hi:[1,0]
	v_pk_mul_f32 v[6:7], v[6:7], v[38:39] op_sel_hi:[1,0]
	v_pk_mul_f32 v[12:13], v[12:13], v[38:39] op_sel_hi:[1,0]
	v_pk_mul_f32 v[10:11], v[10:11], v[38:39] op_sel_hi:[1,0]
	v_pk_mul_f32 v[16:17], v[16:17], v[38:39] op_sel_hi:[1,0]
	v_pk_mul_f32 v[14:15], v[14:15], v[38:39] op_sel_hi:[1,0]
	v_pk_mul_f32 v[20:21], v[20:21], v[38:39] op_sel_hi:[1,0]
	v_pk_mul_f32 v[18:19], v[18:19], v[38:39] op_sel_hi:[1,0]
	v_pk_mul_f32 v[24:25], v[24:25], v[38:39] op_sel_hi:[1,0]
	v_pk_mul_f32 v[22:23], v[22:23], v[38:39] op_sel_hi:[1,0]
	v_pk_mul_f32 v[28:29], v[28:29], v[38:39] op_sel_hi:[1,0]
	v_pk_mul_f32 v[26:27], v[26:27], v[38:39] op_sel_hi:[1,0]
	v_pk_mul_f32 v[32:33], v[32:33], v[38:39] op_sel_hi:[1,0]
	v_pk_mul_f32 v[30:31], v[30:31], v[38:39] op_sel_hi:[1,0]
	ds_write_b128 v50, v[2:5]
	ds_write_b128 v50, v[6:9] offset:1024
	ds_write_b128 v50, v[10:13] offset:2048
	ds_write_b128 v50, v[14:17] offset:3072
	ds_write_b128 v50, v[18:21] offset:4096
	ds_write_b128 v50, v[22:25] offset:5120
	ds_write_b128 v50, v[26:29] offset:6144
	ds_write_b128 v50, v[30:33] offset:7168
	s_waitcnt lgkmcnt(0)
	ds_read_b128 v[18:21], v51
	ds_read_b128 v[22:25], v51 offset:16
	ds_read_b128 v[26:29], v51 offset:32
	ds_read_b128 v[30:33], v51 offset:48
	ds_read_b128 v[52:55], v51 offset:64
	ds_read_b128 v[56:59], v51 offset:80
	ds_read_b128 v[60:63], v51 offset:96
	ds_read_b128 v[64:67], v51 offset:112
	s_waitcnt lgkmcnt(7)
	v_mov_b32_e32 v2, v18
	v_mov_b32_e32 v3, v20
	s_waitcnt lgkmcnt(6)
	v_mov_b32_e32 v4, v22
	v_mov_b32_e32 v5, v24
	s_waitcnt lgkmcnt(5)
	v_mov_b32_e32 v6, v26
	v_mov_b32_e32 v7, v28
	s_waitcnt lgkmcnt(4)
	v_mov_b32_e32 v8, v30
	v_mov_b32_e32 v9, v32
	s_waitcnt lgkmcnt(3)
	v_mov_b32_e32 v10, v52
	v_mov_b32_e32 v11, v54
	s_waitcnt lgkmcnt(2)
	v_mov_b32_e32 v12, v56
	v_mov_b32_e32 v13, v58
	s_waitcnt lgkmcnt(1)
	v_mov_b32_e32 v14, v60
	v_mov_b32_e32 v15, v62
	s_waitcnt lgkmcnt(0)
	v_mov_b32_e32 v16, v64
	v_mov_b32_e32 v17, v66
	v_mov_b32_e32 v18, v19
	v_mov_b32_e32 v19, v21
	v_mov_b32_e32 v20, v23
	v_mov_b32_e32 v21, v25
	v_mov_b32_e32 v22, v27
	v_mov_b32_e32 v23, v29
	v_mov_b32_e32 v24, v31
	v_mov_b32_e32 v25, v33
	v_mov_b32_e32 v26, v53
	v_mov_b32_e32 v27, v55
	v_mov_b32_e32 v28, v57
	v_mov_b32_e32 v29, v59
	v_mov_b32_e32 v30, v61
	v_mov_b32_e32 v31, v63
	v_mov_b32_e32 v32, v65
	v_mov_b32_e32 v33, v67
	v_cvt_scalef32_2xpk16_fp6_f32 v[2:7], v[2:17], v[18:33], 1.0
	global_store_dwordx4 v[36:37], v[2:5], off offset:-8
	global_store_dwordx2 v[36:37], v[6:7], off offset:8
	s_and_saveexec_b64 s[14:15], s[0:1]
	s_cbranch_execz .LBB0_1300
	v_div_scale_f32 v2, s[20:21], v38, v38, 1.0
	v_rcp_f32_e32 v3, v2
	v_div_scale_f32 v4, vcc, 1.0, v38, 1.0
	v_fma_f32 v5, -v2, v3, 1.0
	v_fmac_f32_e32 v3, v5, v3
	v_mul_f32_e32 v5, v4, v3
	v_fma_f32 v6, -v2, v5, v4
	v_fmac_f32_e32 v5, v6, v3
	v_fma_f32 v2, -v2, v5, v4
	v_div_fmas_f32 v2, v2, v3, v5
	v_div_fixup_f32 v2, v2, v38, 1.0
	global_store_dword v42, v2, s[12:13]
	s_branch .LBB0_1300

.LBB0_1487:
	s_cmp_gt_i32 s94, 21
	s_cselect_b64 s[2:3], -1, 0
	s_xor_b64 s[0:1], s[0:1], -1
	s_or_b64 s[0:1], s[2:3], s[0:1]
	s_and_b64 vcc, exec, s[0:1]
	s_cbranch_vccnz .LBB0_1506
	s_add_u32 s22, s82, 0x5400000
	s_addc_u32 s23, s83, 0
	s_add_i32 s8, s93, 0
	s_cmp_lt_i32 s90, 0x8000
	s_cselect_b64 s[0:1], -1, 0
	s_ashr_i32 s91, s90, 31
	v_add_u32_e32 v116, s8, v188
	s_waitcnt vmcnt(0)
	v_add_u32_e32 v2, s8, v189
	s_lshl_b64 s[8:9], s[90:91], 12
	v_add_u32_e32 v117, 0x2400, v2
	v_lshl_or_b32 v2, v206, 6, s8
	v_mov_b32_e32 v3, s9
	s_mov_b64 s[8:9], 0xd400020
	v_lshl_add_u64 v[88:89], v[2:3], 0, s[8:9]
	v_lshlrev_b32_e32 v2, 4, v206
	v_lshlrev_b32_e32 v3, 1, v205
	v_or3_b32 v2, s93, v2, v3
	v_add_u32_e32 v2, 0, v2
	v_add_u32_e32 v118, 0x2400, v2
	v_cndmask_b32_e64 v2, 0, 1, s[0:1]
	v_mbcnt_hi_u32_b32 v111, -1, v208
	s_lshl_b64 s[14:15], s[90:91], 9
	s_ashr_i32 s87, s86, 31
	v_cmp_ne_u32_e64 s[0:1], 1, v2
	v_and_b32_e32 v2, 64, v111
	s_mov_b32 s24, 0
	v_mul_u32_u24_e32 v110, 24, v206
	v_cmp_eq_u32_e64 s[2:3], 0, v210
	v_cmp_eq_u32_e64 s[4:5], 0, v211
	v_cmp_eq_u32_e64 s[6:7], 0, v212
	v_or_b32_e32 v86, s14, v188
	v_mov_b32_e32 v87, s15
	s_lshl_b64 s[12:13], s[86:87], 9
	s_lshl_b64 s[16:17], s[86:87], 12
	s_movk_i32 s25, 0xc0
	s_mov_b64 s[18:19], 0x200
	v_xor_b32_e32 v112, 4, v111
	v_add_u32_e32 v113, 64, v2
	v_xor_b32_e32 v114, 2, v111
	v_xor_b32_e32 v115, 1, v111
	v_readlane_b32 s30, v254, 40
	v_readlane_b32 s31, v254, 41
	s_branch .LBB0_1490

.LBB0_1495:
	ds_read_b128 v[2:5], v123
	ds_read_b128 v[82:85], v123 offset:128
	v_mov_b32_e32 v94, 0
	v_mov_b32_e32 v96, 0
	v_mov_b32_e32 v98, 0
	s_waitcnt lgkmcnt(0)
	v_and_b32_e32 v6, 0xffff, v2
	v_lshrrev_b32_e32 v2, 16, v2
	v_mad_u32_u24 v18, v6, s25, v110
	v_mad_u32_u24 v2, v2, s25, v110
	global_load_dwordx2 v[10:11], v18, s[20:21] offset:16
	global_load_dwordx4 v[6:9], v18, s[20:21]
	global_load_dwordx2 v[16:17], v2, s[20:21] offset:16
	global_load_dwordx4 v[12:15], v2, s[20:21]
	v_and_b32_e32 v2, 0xffff, v3
	v_mad_u32_u24 v2, v2, s25, v110
	global_load_dwordx2 v[130:131], v2, s[20:21] offset:16
	global_load_dwordx4 v[126:129], v2, s[20:21]
	v_lshrrev_b32_e32 v2, 16, v3
	v_mad_u32_u24 v2, v2, s25, v110
	global_load_dwordx2 v[136:137], v2, s[20:21] offset:16
	global_load_dwordx4 v[132:135], v2, s[20:21]
	v_and_b32_e32 v2, 0xffff, v4
	v_mad_u32_u24 v2, v2, s25, v110
	global_load_dwordx2 v[142:143], v2, s[20:21] offset:16
	global_load_dwordx4 v[138:141], v2, s[20:21]
	v_lshrrev_b32_e32 v3, 16, v4
	v_and_b32_e32 v2, 0xffff, v5
	v_lshrrev_b32_e32 v4, 16, v5
	v_mad_u32_u24 v3, v3, s25, v110
	v_mad_u32_u24 v2, v2, s25, v110
	v_mad_u32_u24 v4, v4, s25, v110
	global_load_dwordx2 v[148:149], v3, s[20:21] offset:16
	global_load_dwordx4 v[144:147], v3, s[20:21]
	global_load_dwordx2 v[154:155], v2, s[20:21] offset:16
	global_load_dwordx4 v[150:153], v2, s[20:21]
	global_load_dwordx2 v[160:161], v4, s[20:21] offset:16
	global_load_dwordx4 v[156:159], v4, s[20:21]
	v_mov_b32_e32 v102, 0
	v_mov_b32_e32 v104, 0
	v_mov_b32_e32 v100, 0
	v_mov_b32_e32 v106, 0
	v_mov_b32_e32 v108, 0
	v_mov_b32_e32 v107, 0
	v_mov_b32_e32 v109, 0
	v_mov_b32_e32 v103, 0
	v_mov_b32_e32 v105, 0
	v_mov_b32_e32 v99, 0
	v_mov_b32_e32 v101, 0
	v_mov_b32_e32 v95, 0
	v_mov_b32_e32 v97, 0
	s_and_b64 vcc, exec, s[10:11]
	s_waitcnt vmcnt(14)
	v_cvt_scalef32_pk32_bf16_fp6 v[50:65], v[6:11], 1.0
	v_dot2c_f32_bf16_e32 v106, v50, v78
	s_waitcnt vmcnt(12)
	v_cvt_scalef32_pk32_bf16_fp6 v[34:49], v[12:17], 1.0
	v_dot2c_f32_bf16_e32 v102, v34, v78
	v_dot2c_f32_bf16_e32 v104, v35, v79
	s_waitcnt vmcnt(10)
	v_cvt_scalef32_pk32_bf16_fp6 v[18:33], v[126:131], 1.0
	v_dot2c_f32_bf16_e32 v98, v18, v78
	v_dot2c_f32_bf16_e32 v98, v20, v80
	s_waitcnt vmcnt(8)
	v_cvt_scalef32_pk32_bf16_fp6 v[2:17], v[132:137], 1.0
	v_dot2c_f32_bf16_e32 v94, v2, v78
	v_dot2c_f32_bf16_e32 v96, v3, v79
	v_dot2c_f32_bf16_e32 v94, v4, v80
	v_dot2c_f32_bf16_e32 v96, v5, v81
	v_dot2c_f32_bf16_e32 v94, v6, v74
	v_dot2c_f32_bf16_e32 v96, v7, v75
	v_dot2c_f32_bf16_e32 v94, v8, v76
	v_dot2c_f32_bf16_e32 v96, v9, v77
	v_dot2c_f32_bf16_e32 v94, v10, v70
	v_dot2c_f32_bf16_e32 v96, v11, v71
	v_dot2c_f32_bf16_e32 v94, v12, v72
	v_dot2c_f32_bf16_e32 v96, v13, v73
	v_dot2c_f32_bf16_e32 v94, v14, v66
	v_dot2c_f32_bf16_e32 v96, v15, v67
	v_dot2c_f32_bf16_e32 v94, v16, v68
	v_dot2c_f32_bf16_e32 v96, v17, v69
	s_waitcnt vmcnt(6)
	v_cvt_scalef32_pk32_bf16_fp6 v[2:17], v[138:143], 1.0
	v_mov_b32_e32 v18, 0
	v_mov_b32_e32 v20, 0
	v_dot2c_f32_bf16_e32 v18, v2, v78
	v_dot2c_f32_bf16_e32 v20, v3, v79
	v_dot2c_f32_bf16_e32 v18, v4, v80
	v_dot2c_f32_bf16_e32 v20, v5, v81
	v_dot2c_f32_bf16_e32 v18, v6, v74
	v_dot2c_f32_bf16_e32 v20, v7, v75
	v_dot2c_f32_bf16_e32 v18, v8, v76
	v_dot2c_f32_bf16_e32 v20, v9, v77
	v_dot2c_f32_bf16_e32 v18, v10, v70
	v_dot2c_f32_bf16_e32 v20, v11, v71
	v_dot2c_f32_bf16_e32 v18, v12, v72
	v_dot2c_f32_bf16_e32 v20, v13, v73
	v_dot2c_f32_bf16_e32 v18, v14, v66
	v_dot2c_f32_bf16_e32 v20, v15, v67
	v_dot2c_f32_bf16_e32 v98, v22, v74
	v_dot2c_f32_bf16_e32 v18, v16, v68
	v_dot2c_f32_bf16_e32 v20, v17, v69
	s_waitcnt vmcnt(4)
	v_cvt_scalef32_pk32_bf16_fp6 v[2:17], v[144:149], 1.0
	v_mov_b32_e32 v22, 0
	v_dot2c_f32_bf16_e32 v22, v2, v78
	v_and_b32_e32 v2, 0xffff, v82
	v_dot2c_f32_bf16_e32 v102, v36, v80
	v_dot2c_f32_bf16_e32 v104, v37, v81
	v_mad_u32_u24 v2, v2, s25, v110
	v_dot2c_f32_bf16_e32 v102, v38, v74
	v_dot2c_f32_bf16_e32 v104, v39, v75
	global_load_dwordx2 v[38:39], v2, s[20:21] offset:16
	global_load_dwordx4 v[34:37], v2, s[20:21]
	v_dot2c_f32_bf16_e32 v98, v24, v76
	v_mov_b32_e32 v24, 0
	v_dot2c_f32_bf16_e32 v100, v19, v79
	v_dot2c_f32_bf16_e32 v102, v40, v76
	v_dot2c_f32_bf16_e32 v104, v41, v77
	v_dot2c_f32_bf16_e32 v24, v3, v79
	v_lshrrev_b32_e32 v19, 16, v82
	v_dot2c_f32_bf16_e32 v102, v42, v70
	v_dot2c_f32_bf16_e32 v104, v43, v71
	v_dot2c_f32_bf16_e32 v22, v4, v80
	v_dot2c_f32_bf16_e32 v24, v5, v81
	v_mad_u32_u24 v19, v19, s25, v110
	v_dot2c_f32_bf16_e32 v102, v44, v72
	v_dot2c_f32_bf16_e32 v104, v45, v73
	v_dot2c_f32_bf16_e32 v22, v6, v74
	v_dot2c_f32_bf16_e32 v24, v7, v75
	global_load_dwordx2 v[44:45], v19, s[20:21] offset:16
	global_load_dwordx4 v[40:43], v19, s[20:21]
	v_dot2c_f32_bf16_e32 v22, v8, v76
	v_dot2c_f32_bf16_e32 v24, v9, v77
	v_dot2c_f32_bf16_e32 v22, v10, v70
	v_dot2c_f32_bf16_e32 v24, v11, v71
	v_dot2c_f32_bf16_e32 v22, v12, v72
	v_dot2c_f32_bf16_e32 v24, v13, v73
	v_dot2c_f32_bf16_e32 v98, v26, v70
	v_dot2c_f32_bf16_e32 v22, v14, v66
	v_dot2c_f32_bf16_e32 v24, v15, v67
	v_dot2c_f32_bf16_e32 v98, v28, v72
	v_dot2c_f32_bf16_e32 v22, v16, v68
	v_dot2c_f32_bf16_e32 v24, v17, v69
	s_waitcnt vmcnt(6)
	v_cvt_scalef32_pk32_bf16_fp6 v[2:17], v[150:155], 1.0
	v_mov_b32_e32 v26, 0
	v_mov_b32_e32 v28, 0
	v_dot2c_f32_bf16_e32 v26, v2, v78
	v_dot2c_f32_bf16_e32 v28, v3, v79
	v_and_b32_e32 v2, 0xffff, v83
	v_dot2c_f32_bf16_e32 v102, v46, v66
	v_dot2c_f32_bf16_e32 v104, v47, v67
	v_dot2c_f32_bf16_e32 v26, v4, v80
	v_dot2c_f32_bf16_e32 v28, v5, v81
	v_mad_u32_u24 v2, v2, s25, v110
	v_dot2c_f32_bf16_e32 v108, v51, v79
	v_dot2c_f32_bf16_e32 v102, v48, v68
	v_dot2c_f32_bf16_e32 v104, v49, v69
	v_dot2c_f32_bf16_e32 v26, v6, v74
	v_dot2c_f32_bf16_e32 v28, v7, v75
	global_load_dwordx2 v[50:51], v2, s[20:21] offset:16
	global_load_dwordx4 v[46:49], v2, s[20:21]
	v_dot2c_f32_bf16_e32 v26, v8, v76
	v_dot2c_f32_bf16_e32 v28, v9, v77
	v_dot2c_f32_bf16_e32 v26, v10, v70
	v_dot2c_f32_bf16_e32 v28, v11, v71
	v_dot2c_f32_bf16_e32 v26, v12, v72
	v_dot2c_f32_bf16_e32 v28, v13, v73
	v_dot2c_f32_bf16_e32 v26, v14, v66
	v_dot2c_f32_bf16_e32 v28, v15, v67
	v_dot2c_f32_bf16_e32 v98, v30, v66
	v_dot2c_f32_bf16_e32 v26, v16, v68
	v_dot2c_f32_bf16_e32 v28, v17, v69
	s_waitcnt vmcnt(6)
	v_cvt_scalef32_pk32_bf16_fp6 v[2:17], v[156:161], 1.0
	v_mov_b32_e32 v30, 0
	v_dot2c_f32_bf16_e32 v106, v52, v80
	v_dot2c_f32_bf16_e32 v108, v53, v81
	v_dot2c_f32_bf16_e32 v30, v2, v78
	v_lshrrev_b32_e32 v2, 16, v83
	v_dot2c_f32_bf16_e32 v106, v54, v74
	v_dot2c_f32_bf16_e32 v108, v55, v75
	v_mad_u32_u24 v2, v2, s25, v110
	v_dot2c_f32_bf16_e32 v106, v56, v76
	v_dot2c_f32_bf16_e32 v108, v57, v77
	global_load_dwordx2 v[56:57], v2, s[20:21] offset:16
	global_load_dwordx4 v[52:55], v2, s[20:21]
	v_dot2c_f32_bf16_e32 v106, v58, v70
	v_dot2c_f32_bf16_e32 v108, v59, v71
	v_and_b32_e32 v2, 0xffff, v84
	v_dot2c_f32_bf16_e32 v106, v60, v72
	v_dot2c_f32_bf16_e32 v108, v61, v73
	v_mad_u32_u24 v2, v2, s25, v110
	v_dot2c_f32_bf16_e32 v106, v62, v66
	v_dot2c_f32_bf16_e32 v108, v63, v67
	global_load_dwordx2 v[62:63], v2, s[20:21] offset:16
	global_load_dwordx4 v[58:61], v2, s[20:21]
	v_lshrrev_b32_e32 v2, 16, v84
	v_mad_u32_u24 v2, v2, s25, v110
	global_load_dwordx2 v[130:131], v2, s[20:21] offset:16
	global_load_dwordx4 v[126:129], v2, s[20:21]
	v_and_b32_e32 v2, 0xffff, v85
	v_mad_u32_u24 v2, v2, s25, v110
	global_load_dwordx2 v[136:137], v2, s[20:21] offset:16
	global_load_dwordx4 v[132:135], v2, s[20:21]
	v_lshrrev_b32_e32 v2, 16, v85
	v_mad_u32_u24 v2, v2, s25, v110
	global_load_dwordx2 v[142:143], v2, s[20:21] offset:16
	global_load_dwordx4 v[138:141], v2, s[20:21]
	v_dot2c_f32_bf16_e32 v98, v32, v68
	v_mov_b32_e32 v32, 0
	v_dot2c_f32_bf16_e32 v32, v3, v79
	v_dot2c_f32_bf16_e32 v30, v4, v80
	v_dot2c_f32_bf16_e32 v32, v5, v81
	v_dot2c_f32_bf16_e32 v30, v6, v74
	v_dot2c_f32_bf16_e32 v32, v7, v75
	v_dot2c_f32_bf16_e32 v30, v8, v76
	v_dot2c_f32_bf16_e32 v32, v9, v77
	v_dot2c_f32_bf16_e32 v30, v10, v70
	v_dot2c_f32_bf16_e32 v32, v11, v71
	v_dot2c_f32_bf16_e32 v30, v12, v72
	v_dot2c_f32_bf16_e32 v32, v13, v73
	v_dot2c_f32_bf16_e32 v30, v14, v66
	v_dot2c_f32_bf16_e32 v32, v15, v67
	v_dot2c_f32_bf16_e32 v30, v16, v68
	v_dot2c_f32_bf16_e32 v32, v17, v69
	s_waitcnt vmcnt(14)
	v_cvt_scalef32_pk32_bf16_fp6 v[2:17], v[34:39], 1.0
	v_dot2c_f32_bf16_e32 v107, v2, v78
	v_dot2c_f32_bf16_e32 v109, v3, v79
	v_dot2c_f32_bf16_e32 v107, v4, v80
	v_dot2c_f32_bf16_e32 v109, v5, v81
	v_dot2c_f32_bf16_e32 v107, v6, v74
	v_dot2c_f32_bf16_e32 v109, v7, v75
	v_dot2c_f32_bf16_e32 v107, v8, v76
	v_dot2c_f32_bf16_e32 v109, v9, v77
	v_dot2c_f32_bf16_e32 v107, v10, v70
	v_dot2c_f32_bf16_e32 v109, v11, v71
	v_dot2c_f32_bf16_e32 v107, v12, v72
	v_dot2c_f32_bf16_e32 v109, v13, v73
	v_dot2c_f32_bf16_e32 v107, v14, v66
	v_dot2c_f32_bf16_e32 v109, v15, v67
	v_dot2c_f32_bf16_e32 v107, v16, v68
	v_dot2c_f32_bf16_e32 v109, v17, v69
	s_waitcnt vmcnt(12)
	v_cvt_scalef32_pk32_bf16_fp6 v[2:17], v[40:45], 1.0
	v_dot2c_f32_bf16_e32 v103, v2, v78
	v_dot2c_f32_bf16_e32 v105, v3, v79
	v_dot2c_f32_bf16_e32 v103, v4, v80
	v_dot2c_f32_bf16_e32 v105, v5, v81
	v_dot2c_f32_bf16_e32 v103, v6, v74
	v_dot2c_f32_bf16_e32 v105, v7, v75
	v_dot2c_f32_bf16_e32 v103, v8, v76
	v_dot2c_f32_bf16_e32 v105, v9, v77
	v_dot2c_f32_bf16_e32 v103, v10, v70
	v_dot2c_f32_bf16_e32 v105, v11, v71
	v_dot2c_f32_bf16_e32 v103, v12, v72
	v_dot2c_f32_bf16_e32 v105, v13, v73
	v_dot2c_f32_bf16_e32 v103, v14, v66
	v_dot2c_f32_bf16_e32 v105, v15, v67
	v_dot2c_f32_bf16_e32 v103, v16, v68
	v_dot2c_f32_bf16_e32 v105, v17, v69
	s_waitcnt vmcnt(10)
	v_cvt_scalef32_pk32_bf16_fp6 v[2:17], v[46:51], 1.0
	v_dot2c_f32_bf16_e32 v99, v2, v78
	v_dot2c_f32_bf16_e32 v101, v3, v79
	v_dot2c_f32_bf16_e32 v99, v4, v80
	v_dot2c_f32_bf16_e32 v101, v5, v81
	v_dot2c_f32_bf16_e32 v99, v6, v74
	v_dot2c_f32_bf16_e32 v101, v7, v75
	v_dot2c_f32_bf16_e32 v99, v8, v76
	v_dot2c_f32_bf16_e32 v101, v9, v77
	v_dot2c_f32_bf16_e32 v99, v10, v70
	v_dot2c_f32_bf16_e32 v101, v11, v71
	v_dot2c_f32_bf16_e32 v99, v12, v72
	v_dot2c_f32_bf16_e32 v101, v13, v73
	v_dot2c_f32_bf16_e32 v99, v14, v66
	v_dot2c_f32_bf16_e32 v101, v15, v67
	v_dot2c_f32_bf16_e32 v99, v16, v68
	v_dot2c_f32_bf16_e32 v101, v17, v69
	s_waitcnt vmcnt(8)
	v_cvt_scalef32_pk32_bf16_fp6 v[2:17], v[52:57], 1.0
	v_dot2c_f32_bf16_e32 v95, v2, v78
	v_dot2c_f32_bf16_e32 v97, v3, v79
	v_dot2c_f32_bf16_e32 v95, v4, v80
	v_dot2c_f32_bf16_e32 v97, v5, v81
	v_dot2c_f32_bf16_e32 v95, v6, v74
	v_dot2c_f32_bf16_e32 v97, v7, v75
	v_dot2c_f32_bf16_e32 v95, v8, v76
	v_dot2c_f32_bf16_e32 v97, v9, v77
	v_dot2c_f32_bf16_e32 v95, v10, v70
	v_dot2c_f32_bf16_e32 v97, v11, v71
	v_dot2c_f32_bf16_e32 v95, v12, v72
	v_dot2c_f32_bf16_e32 v97, v13, v73
	v_dot2c_f32_bf16_e32 v95, v14, v66
	v_dot2c_f32_bf16_e32 v97, v15, v67
	v_dot2c_f32_bf16_e32 v100, v21, v81
	v_dot2c_f32_bf16_e32 v95, v16, v68
	v_dot2c_f32_bf16_e32 v97, v17, v69
	s_waitcnt vmcnt(6)
	v_cvt_scalef32_pk32_bf16_fp6 v[2:17], v[58:63], 1.0
	v_mov_b32_e32 v19, 0
	v_mov_b32_e32 v21, 0
	v_dot2c_f32_bf16_e32 v19, v2, v78
	v_dot2c_f32_bf16_e32 v21, v3, v79
	v_dot2c_f32_bf16_e32 v19, v4, v80
	v_dot2c_f32_bf16_e32 v21, v5, v81
	v_dot2c_f32_bf16_e32 v19, v6, v74
	v_dot2c_f32_bf16_e32 v21, v7, v75
	v_dot2c_f32_bf16_e32 v19, v8, v76
	v_dot2c_f32_bf16_e32 v21, v9, v77
	v_dot2c_f32_bf16_e32 v19, v10, v70
	v_dot2c_f32_bf16_e32 v21, v11, v71
	v_dot2c_f32_bf16_e32 v19, v12, v72
	v_dot2c_f32_bf16_e32 v21, v13, v73
	v_dot2c_f32_bf16_e32 v100, v23, v75
	v_dot2c_f32_bf16_e32 v19, v14, v66
	v_dot2c_f32_bf16_e32 v21, v15, v67
	v_dot2c_f32_bf16_e32 v100, v25, v77
	v_dot2c_f32_bf16_e32 v19, v16, v68
	v_dot2c_f32_bf16_e32 v21, v17, v69
	s_waitcnt vmcnt(4)
	v_cvt_scalef32_pk32_bf16_fp6 v[2:17], v[126:131], 1.0
	v_mov_b32_e32 v23, 0
	v_mov_b32_e32 v25, 0
	v_dot2c_f32_bf16_e32 v23, v2, v78
	v_dot2c_f32_bf16_e32 v25, v3, v79
	v_dot2c_f32_bf16_e32 v23, v4, v80
	v_dot2c_f32_bf16_e32 v25, v5, v81
	v_dot2c_f32_bf16_e32 v23, v6, v74
	v_dot2c_f32_bf16_e32 v25, v7, v75
	v_dot2c_f32_bf16_e32 v23, v8, v76
	v_dot2c_f32_bf16_e32 v25, v9, v77
	v_dot2c_f32_bf16_e32 v23, v10, v70
	v_dot2c_f32_bf16_e32 v25, v11, v71
	v_dot2c_f32_bf16_e32 v23, v12, v72
	v_dot2c_f32_bf16_e32 v25, v13, v73
	v_dot2c_f32_bf16_e32 v100, v27, v71
	v_dot2c_f32_bf16_e32 v23, v14, v66
	v_dot2c_f32_bf16_e32 v25, v15, v67
	v_dot2c_f32_bf16_e32 v100, v29, v73
	v_dot2c_f32_bf16_e32 v23, v16, v68
	v_dot2c_f32_bf16_e32 v25, v17, v69
	s_waitcnt vmcnt(2)
	v_cvt_scalef32_pk32_bf16_fp6 v[2:17], v[132:137], 1.0
	v_mov_b32_e32 v27, 0
	v_mov_b32_e32 v29, 0
	v_dot2c_f32_bf16_e32 v27, v2, v78
	v_dot2c_f32_bf16_e32 v29, v3, v79
	v_dot2c_f32_bf16_e32 v27, v4, v80
	v_dot2c_f32_bf16_e32 v29, v5, v81
	v_dot2c_f32_bf16_e32 v27, v6, v74
	v_dot2c_f32_bf16_e32 v29, v7, v75
	v_dot2c_f32_bf16_e32 v27, v8, v76
	v_dot2c_f32_bf16_e32 v29, v9, v77
	v_dot2c_f32_bf16_e32 v27, v10, v70
	v_dot2c_f32_bf16_e32 v29, v11, v71
	v_dot2c_f32_bf16_e32 v27, v12, v72
	v_dot2c_f32_bf16_e32 v29, v13, v73
	v_dot2c_f32_bf16_e32 v100, v31, v67
	v_dot2c_f32_bf16_e32 v27, v14, v66
	v_dot2c_f32_bf16_e32 v29, v15, v67
	v_dot2c_f32_bf16_e32 v100, v33, v69
	v_dot2c_f32_bf16_e32 v27, v16, v68
	v_dot2c_f32_bf16_e32 v29, v17, v69
	s_waitcnt vmcnt(0)
	v_cvt_scalef32_pk32_bf16_fp6 v[2:17], v[138:143], 1.0
	v_mov_b32_e32 v31, 0
	v_mov_b32_e32 v33, 0
	v_dot2c_f32_bf16_e32 v31, v2, v78
	v_dot2c_f32_bf16_e32 v33, v3, v79
	v_dot2c_f32_bf16_e32 v31, v4, v80
	v_dot2c_f32_bf16_e32 v33, v5, v81
	v_dot2c_f32_bf16_e32 v31, v6, v74
	v_dot2c_f32_bf16_e32 v33, v7, v75
	v_dot2c_f32_bf16_e32 v31, v8, v76
	v_dot2c_f32_bf16_e32 v33, v9, v77
	v_dot2c_f32_bf16_e32 v31, v10, v70
	v_dot2c_f32_bf16_e32 v33, v11, v71
	v_dot2c_f32_bf16_e32 v31, v12, v72
	v_dot2c_f32_bf16_e32 v33, v13, v73
	v_dot2c_f32_bf16_e32 v31, v14, v66
	v_dot2c_f32_bf16_e32 v33, v15, v67
	v_pk_add_f32 v[8:9], v[104:105], v[102:103]
	v_pk_add_f32 v[10:11], v[24:25], v[22:23]
	v_dot2c_f32_bf16_e32 v31, v16, v68
	v_dot2c_f32_bf16_e32 v33, v17, v69
	v_cndmask_b32_e64 v7, v8, v10, s[2:3]
	v_pk_add_f32 v[14:15], v[100:101], v[98:99]
	v_pk_add_f32 v[16:17], v[28:29], v[26:27]
	v_dot2c_f32_bf16_e32 v106, v64, v68
	v_dot2c_f32_bf16_e32 v108, v65, v69
	v_pk_add_f32 v[4:5], v[20:21], v[18:19]
	ds_bpermute_b32 v12, v119, v7
	v_cndmask_b32_e64 v7, v14, v16, s[2:3]
	v_pk_add_f32 v[20:21], v[96:97], v[94:95]
	v_pk_add_f32 v[22:23], v[32:33], v[30:31]
	v_pk_add_f32 v[2:3], v[108:109], v[106:107]
	ds_bpermute_b32 v18, v119, v7
	v_cndmask_b32_e64 v7, v20, v22, s[2:3]
	v_cndmask_b32_e64 v6, v2, v4, s[2:3]
	ds_bpermute_b32 v24, v119, v7
	v_cndmask_b32_e64 v7, v3, v5, s[2:3]
	ds_bpermute_b32 v6, v119, v6
	ds_bpermute_b32 v7, v119, v7
	v_cndmask_b32_e64 v3, v5, v3, s[2:3]
	v_cndmask_b32_e64 v2, v4, v2, s[2:3]
	v_cndmask_b32_e64 v5, v15, v17, s[2:3]
	ds_bpermute_b32 v19, v119, v5
	s_waitcnt lgkmcnt(1)
	v_pk_add_f32 v[2:3], v[2:3], v[6:7]
	v_cndmask_b32_e64 v7, v9, v11, s[2:3]
	ds_bpermute_b32 v13, v119, v7
	v_cndmask_b32_e64 v7, v21, v23, s[2:3]
	ds_bpermute_b32 v25, v119, v7
	v_cndmask_b32_e64 v9, v11, v9, s[2:3]
	v_cndmask_b32_e64 v8, v10, v8, s[2:3]
	v_cndmask_b32_e64 v11, v23, v21, s[2:3]
	v_cndmask_b32_e64 v10, v22, v20, s[2:3]
	v_cndmask_b32_e64 v5, v17, v15, s[2:3]
	v_cndmask_b32_e64 v4, v16, v14, s[2:3]
	s_waitcnt lgkmcnt(1)
	v_pk_add_f32 v[8:9], v[8:9], v[12:13]
	s_waitcnt lgkmcnt(0)
	v_pk_add_f32 v[10:11], v[10:11], v[24:25]
	v_pk_add_f32 v[4:5], v[4:5], v[18:19]
	v_cndmask_b32_e64 v7, v8, v10, s[4:5]
	v_cndmask_b32_e64 v6, v2, v4, s[4:5]
	ds_bpermute_b32 v12, v120, v7
	v_cndmask_b32_e64 v7, v3, v5, s[4:5]
	v_cndmask_b32_e64 v3, v5, v3, s[4:5]
	v_cndmask_b32_e64 v5, v9, v11, s[4:5]
	ds_bpermute_b32 v6, v120, v6
	ds_bpermute_b32 v7, v120, v7
	ds_bpermute_b32 v13, v120, v5
	v_cndmask_b32_e64 v2, v4, v2, s[4:5]
	v_cndmask_b32_e64 v5, v11, v9, s[4:5]
	v_cndmask_b32_e64 v4, v10, v8, s[4:5]
	s_waitcnt lgkmcnt(1)
	v_pk_add_f32 v[2:3], v[2:3], v[6:7]
	s_waitcnt lgkmcnt(0)
	v_pk_add_f32 v[4:5], v[4:5], v[12:13]
	s_nop 0
	v_cndmask_b32_e64 v6, v2, v4, s[6:7]
	v_cndmask_b32_e64 v7, v3, v5, s[6:7]
	ds_bpermute_b32 v6, v121, v6
	ds_bpermute_b32 v7, v121, v7
	v_cndmask_b32_e64 v3, v5, v3, s[6:7]
	v_cndmask_b32_e64 v2, v4, v2, s[6:7]
	s_waitcnt lgkmcnt(0)
	v_pk_add_f32 v[2:3], v[2:3], v[6:7]
	s_cbranch_vccnz .LBB0_1492
	ds_read2st64_b32 v[4:5], v124 offset1:1
	s_waitcnt lgkmcnt(0)
	v_pk_add_f32 v[2:3], v[2:3], v[4:5]
	s_branch .LBB0_1492

.LBB0_1504:
	v_add_u32_e32 v0, s93, v98
	ds_read_b128 v[12:15], v0
	ds_read_b128 v[64:67], v0 offset:128
	v_add_u32_e32 v85, s93, v96
	s_ashr_i32 s22, s18, 11
	s_mul_hi_i32 s23, s22, 0xc000
	s_waitcnt lgkmcnt(0)
	v_and_b32_e32 v0, 0xffff, v12
	v_lshrrev_b32_e32 v1, 16, v12
	v_mad_u32_u24 v12, v0, s26, v110
	v_mad_u32_u24 v16, v1, s26, v110
	global_load_dwordx2 v[4:5], v12, s[14:15] offset:16
	global_load_dwordx4 v[0:3], v12, s[14:15]
	global_load_dwordx2 v[10:11], v16, s[14:15] offset:16
	global_load_dwordx4 v[6:9], v16, s[14:15]
	v_and_b32_e32 v12, 0xffff, v13
	v_mad_u32_u24 v12, v12, s26, v110
	global_load_dwordx2 v[104:105], v12, s[14:15] offset:16
	global_load_dwordx4 v[100:103], v12, s[14:15]
	v_lshrrev_b32_e32 v12, 16, v13
	v_mad_u32_u24 v12, v12, s26, v110
	global_load_dwordx2 v[120:121], v12, s[14:15] offset:16
	global_load_dwordx4 v[116:119], v12, s[14:15]
	v_and_b32_e32 v12, 0xffff, v14
	v_mad_u32_u24 v12, v12, s26, v110
	ds_read_b128 v[106:109], v85
	ds_read_b128 v[146:149], v85 offset:16
	global_load_dwordx2 v[126:127], v12, s[14:15] offset:16
	global_load_dwordx4 v[122:125], v12, s[14:15]
	v_lshrrev_b32_e32 v13, 16, v14
	v_and_b32_e32 v12, 0xffff, v15
	v_lshrrev_b32_e32 v14, 16, v15
	v_mad_u32_u24 v13, v13, s26, v110
	v_mad_u32_u24 v12, v12, s26, v110
	v_mad_u32_u24 v14, v14, s26, v110
	global_load_dwordx2 v[132:133], v13, s[14:15] offset:16
	global_load_dwordx4 v[128:131], v13, s[14:15]
	global_load_dwordx2 v[138:139], v12, s[14:15] offset:16
	global_load_dwordx4 v[134:137], v12, s[14:15]
	global_load_dwordx2 v[144:145], v14, s[14:15] offset:16
	global_load_dwordx4 v[140:143], v14, s[14:15]
	s_mul_i32 s22, s22, 0xc000
	s_add_u32 s28, s82, s22
	s_addc_u32 s29, s83, s23
	s_lshl_b64 s[22:23], s[20:21], 12
	s_add_u32 s22, s30, s22
	s_addc_u32 s23, s31, s23
	s_waitcnt vmcnt(14)
	v_cvt_scalef32_pk32_f16_fp6 v[48:63], v[0:5], 1.0
	s_waitcnt lgkmcnt(1)
	v_pk_fma_f16 v48, v106, v48, 0
	s_waitcnt vmcnt(12)
	v_cvt_scalef32_pk32_f16_fp6 v[32:47], v[6:11], 1.0
	v_pk_fma_f16 v49, v106, v49, 0
	v_pk_fma_f16 v50, v106, v50, 0
	v_pk_fma_f16 v51, v106, v51, 0
	v_pk_fma_f16 v52, v106, v52, 0
	v_pk_fma_f16 v53, v106, v53, 0
	v_pk_fma_f16 v54, v106, v54, 0
	v_pk_fma_f16 v55, v106, v55, 0
	v_pk_fma_f16 v56, v106, v56, 0
	v_pk_fma_f16 v57, v106, v57, 0
	v_pk_fma_f16 v58, v106, v58, 0
	v_pk_fma_f16 v59, v106, v59, 0
	v_pk_fma_f16 v60, v106, v60, 0
	v_pk_fma_f16 v61, v106, v61, 0
	v_pk_fma_f16 v62, v106, v62, 0
	v_pk_fma_f16 v63, v106, v63, 0
	s_waitcnt vmcnt(10)
	v_cvt_scalef32_pk32_f16_fp6 v[16:31], v[100:105], 1.0
	v_pk_fma_f16 v32, v107, v32, v48
	v_pk_fma_f16 v33, v107, v33, v49
	v_pk_fma_f16 v34, v107, v34, v50
	v_pk_fma_f16 v35, v107, v35, v51
	v_pk_fma_f16 v36, v107, v36, v52
	v_pk_fma_f16 v37, v107, v37, v53
	v_pk_fma_f16 v38, v107, v38, v54
	v_pk_fma_f16 v39, v107, v39, v55
	v_pk_fma_f16 v40, v107, v40, v56
	v_pk_fma_f16 v41, v107, v41, v57
	v_pk_fma_f16 v42, v107, v42, v58
	v_pk_fma_f16 v43, v107, v43, v59
	v_pk_fma_f16 v44, v107, v44, v60
	v_pk_fma_f16 v45, v107, v45, v61
	v_pk_fma_f16 v46, v107, v46, v62
	v_pk_fma_f16 v47, v107, v47, v63
	s_waitcnt vmcnt(8)
	v_cvt_scalef32_pk32_f16_fp6 v[0:15], v[116:121], 1.0
	v_pk_fma_f16 v16, v108, v16, v32
	v_pk_fma_f16 v17, v108, v17, v33
	v_pk_fma_f16 v18, v108, v18, v34
	v_pk_fma_f16 v19, v108, v19, v35
	v_pk_fma_f16 v20, v108, v20, v36
	v_pk_fma_f16 v21, v108, v21, v37
	v_pk_fma_f16 v22, v108, v22, v38
	v_pk_fma_f16 v23, v108, v23, v39
	v_pk_fma_f16 v24, v108, v24, v40
	v_pk_fma_f16 v25, v108, v25, v41
	v_pk_fma_f16 v26, v108, v26, v42
	v_pk_fma_f16 v27, v108, v27, v43
	v_pk_fma_f16 v28, v108, v28, v44
	v_pk_fma_f16 v29, v108, v29, v45
	v_pk_fma_f16 v30, v108, v30, v46
	v_pk_fma_f16 v31, v108, v31, v47
	v_pk_fma_f16 v16, v109, v0, v16
	v_pk_fma_f16 v17, v109, v1, v17
	v_pk_fma_f16 v18, v109, v2, v18
	v_pk_fma_f16 v19, v109, v3, v19
	v_pk_fma_f16 v20, v109, v4, v20
	v_pk_fma_f16 v21, v109, v5, v21
	v_pk_fma_f16 v22, v109, v6, v22
	v_pk_fma_f16 v23, v109, v7, v23
	v_pk_fma_f16 v24, v109, v8, v24
	v_pk_fma_f16 v25, v109, v9, v25
	v_pk_fma_f16 v26, v109, v10, v26
	v_pk_fma_f16 v27, v109, v11, v27
	v_pk_fma_f16 v28, v109, v12, v28
	v_pk_fma_f16 v29, v109, v13, v29
	v_pk_fma_f16 v30, v109, v14, v30
	v_pk_fma_f16 v31, v109, v15, v31
	s_waitcnt vmcnt(6)
	v_cvt_scalef32_pk32_f16_fp6 v[0:15], v[122:127], 1.0
	s_waitcnt lgkmcnt(0)
	v_pk_fma_f16 v16, v146, v0, v16
	v_pk_fma_f16 v17, v146, v1, v17
	v_pk_fma_f16 v18, v146, v2, v18
	v_pk_fma_f16 v19, v146, v3, v19
	v_pk_fma_f16 v32, v146, v4, v20
	v_pk_fma_f16 v33, v146, v5, v21
	v_pk_fma_f16 v34, v146, v6, v22
	v_pk_fma_f16 v35, v146, v7, v23
	v_pk_fma_f16 v36, v146, v8, v24
	v_pk_fma_f16 v37, v146, v9, v25
	v_pk_fma_f16 v26, v146, v10, v26
	v_pk_fma_f16 v27, v146, v11, v27
	v_pk_fma_f16 v28, v146, v12, v28
	v_pk_fma_f16 v29, v146, v13, v29
	v_pk_fma_f16 v38, v146, v14, v30
	v_pk_fma_f16 v39, v146, v15, v31
	s_waitcnt vmcnt(4)
	v_cvt_scalef32_pk32_f16_fp6 v[0:15], v[128:133], 1.0
	v_pk_fma_f16 v16, v147, v0, v16
	v_and_b32_e32 v0, 0xffff, v64
	v_mad_u32_u24 v0, v0, s26, v110
	global_load_dwordx2 v[24:25], v0, s[14:15] offset:16
	global_load_dwordx4 v[20:23], v0, s[14:15]
	v_lshrrev_b32_e32 v0, 16, v64
	v_mad_u32_u24 v0, v0, s26, v110
	v_pk_fma_f16 v17, v147, v1, v17
	v_pk_fma_f16 v18, v147, v2, v18
	v_pk_fma_f16 v19, v147, v3, v19
	v_pk_fma_f16 v32, v147, v4, v32
	v_pk_fma_f16 v33, v147, v5, v33
	v_pk_fma_f16 v34, v147, v6, v34
	v_pk_fma_f16 v35, v147, v7, v35
	v_pk_fma_f16 v36, v147, v8, v36
	v_pk_fma_f16 v37, v147, v9, v37
	v_pk_fma_f16 v40, v147, v10, v26
	v_pk_fma_f16 v41, v147, v11, v27
	v_pk_fma_f16 v42, v147, v12, v28
	v_pk_fma_f16 v43, v147, v13, v29
	global_load_dwordx2 v[30:31], v0, s[14:15] offset:16
	global_load_dwordx4 v[26:29], v0, s[14:15]
	v_pk_fma_f16 v38, v147, v14, v38
	v_pk_fma_f16 v39, v147, v15, v39
	s_waitcnt vmcnt(6)
	v_cvt_scalef32_pk32_f16_fp6 v[0:15], v[134:139], 1.0
	v_pk_fma_f16 v16, v148, v0, v16
	v_and_b32_e32 v0, 0xffff, v65
	v_mad_u32_u24 v0, v0, s26, v110
	v_pk_fma_f16 v17, v148, v1, v17
	v_pk_fma_f16 v18, v148, v2, v18
	v_pk_fma_f16 v19, v148, v3, v19
	v_pk_fma_f16 v44, v148, v4, v32
	v_pk_fma_f16 v45, v148, v5, v33
	v_pk_fma_f16 v46, v148, v6, v34
	v_pk_fma_f16 v47, v148, v7, v35
	v_pk_fma_f16 v48, v148, v8, v36
	v_pk_fma_f16 v49, v148, v9, v37
	global_load_dwordx2 v[36:37], v0, s[14:15] offset:16
	global_load_dwordx4 v[32:35], v0, s[14:15]
	v_pk_fma_f16 v50, v148, v10, v40
	v_pk_fma_f16 v51, v148, v11, v41
	v_pk_fma_f16 v52, v148, v12, v42
	v_pk_fma_f16 v53, v148, v13, v43
	v_pk_fma_f16 v54, v148, v14, v38
	v_pk_fma_f16 v55, v148, v15, v39
	s_waitcnt vmcnt(6)
	v_cvt_scalef32_pk32_f16_fp6 v[0:15], v[140:145], 1.0
	v_pk_fma_f16 v104, v149, v0, v16
	v_lshrrev_b32_e32 v0, 16, v65
	v_mad_u32_u24 v0, v0, s26, v110
	global_load_dwordx2 v[42:43], v0, s[14:15] offset:16
	global_load_dwordx4 v[38:41], v0, s[14:15]
	v_and_b32_e32 v0, 0xffff, v66
	v_mad_u32_u24 v0, v0, s26, v110
	v_pk_fma_f16 v105, v149, v1, v17
	v_pk_fma_f16 v106, v149, v2, v18
	v_pk_fma_f16 v107, v149, v3, v19
	v_pk_fma_f16 v108, v149, v4, v44
	v_pk_fma_f16 v109, v149, v5, v45
	v_pk_fma_f16 v116, v149, v6, v46
	v_pk_fma_f16 v117, v149, v7, v47
	v_pk_fma_f16 v118, v149, v8, v48
	v_pk_fma_f16 v119, v149, v9, v49
	ds_read_b128 v[100:103], v85 offset:256
	ds_read_b128 v[16:19], v85 offset:272
	global_load_dwordx2 v[48:49], v0, s[14:15] offset:16
	global_load_dwordx4 v[44:47], v0, s[14:15]
	v_lshrrev_b32_e32 v0, 16, v66
	v_mad_u32_u24 v0, v0, s26, v110
	v_pk_fma_f16 v120, v149, v10, v50
	v_pk_fma_f16 v121, v149, v11, v51
	v_pk_fma_f16 v122, v149, v12, v52
	v_pk_fma_f16 v123, v149, v13, v53
	v_pk_fma_f16 v124, v149, v14, v54
	v_pk_fma_f16 v125, v149, v15, v55
	global_load_dwordx2 v[54:55], v0, s[14:15] offset:16
	global_load_dwordx4 v[50:53], v0, s[14:15]
	v_and_b32_e32 v0, 0xffff, v67
	v_mad_u32_u24 v0, v0, s26, v110
	global_load_dwordx2 v[60:61], v0, s[14:15] offset:16
	global_load_dwordx4 v[56:59], v0, s[14:15]
	v_lshrrev_b32_e32 v0, 16, v67
	v_mad_u32_u24 v0, v0, s26, v110
	global_load_dwordx2 v[66:67], v0, s[14:15] offset:16
	global_load_dwordx4 v[62:65], v0, s[14:15]
	s_waitcnt vmcnt(14)
	v_cvt_scalef32_pk32_f16_fp6 v[0:15], v[20:25], 1.0
	s_waitcnt lgkmcnt(1)
	v_pk_fma_f16 v20, v100, v0, v104
	v_pk_fma_f16 v21, v100, v1, v105
	v_pk_fma_f16 v22, v100, v2, v106
	v_pk_fma_f16 v23, v100, v3, v107
	v_pk_fma_f16 v24, v100, v4, v108
	v_pk_fma_f16 v25, v100, v5, v109
	v_pk_fma_f16 v85, v100, v6, v116
	v_pk_fma_f16 v104, v100, v7, v117
	v_pk_fma_f16 v105, v100, v8, v118
	v_pk_fma_f16 v106, v100, v9, v119
	v_pk_fma_f16 v107, v100, v10, v120
	v_pk_fma_f16 v108, v100, v11, v121
	v_pk_fma_f16 v109, v100, v12, v122
	v_pk_fma_f16 v116, v100, v13, v123
	v_pk_fma_f16 v117, v100, v14, v124
	v_pk_fma_f16 v100, v100, v15, v125
	s_waitcnt vmcnt(12)
	v_cvt_scalef32_pk32_f16_fp6 v[0:15], v[26:31], 1.0
	v_pk_fma_f16 v20, v101, v0, v20
	v_pk_fma_f16 v21, v101, v1, v21
	v_pk_fma_f16 v22, v101, v2, v22
	v_pk_fma_f16 v23, v101, v3, v23
	v_pk_fma_f16 v24, v101, v4, v24
	v_pk_fma_f16 v25, v101, v5, v25
	v_pk_fma_f16 v26, v101, v6, v85
	v_pk_fma_f16 v27, v101, v7, v104
	v_pk_fma_f16 v28, v101, v8, v105
	v_pk_fma_f16 v29, v101, v9, v106
	v_pk_fma_f16 v30, v101, v10, v107
	v_pk_fma_f16 v31, v101, v11, v108
	v_pk_fma_f16 v85, v101, v12, v109
	v_pk_fma_f16 v104, v101, v13, v116
	v_pk_fma_f16 v105, v101, v14, v117
	v_pk_fma_f16 v100, v101, v15, v100
	s_waitcnt vmcnt(10)
	v_cvt_scalef32_pk32_f16_fp6 v[0:15], v[32:37], 1.0
	v_pk_fma_f16 v20, v102, v0, v20
	v_pk_fma_f16 v21, v102, v1, v21
	v_pk_fma_f16 v22, v102, v2, v22
	v_pk_fma_f16 v23, v102, v3, v23
	v_pk_fma_f16 v24, v102, v4, v24
	v_pk_fma_f16 v25, v102, v5, v25
	v_pk_fma_f16 v26, v102, v6, v26
	v_pk_fma_f16 v27, v102, v7, v27
	v_pk_fma_f16 v28, v102, v8, v28
	v_pk_fma_f16 v29, v102, v9, v29
	v_pk_fma_f16 v30, v102, v10, v30
	v_pk_fma_f16 v31, v102, v11, v31
	v_pk_fma_f16 v32, v102, v12, v85
	v_pk_fma_f16 v33, v102, v13, v104
	v_pk_fma_f16 v34, v102, v14, v105
	v_pk_fma_f16 v35, v102, v15, v100
	s_waitcnt vmcnt(8)
	v_cvt_scalef32_pk32_f16_fp6 v[0:15], v[38:43], 1.0
	v_pk_fma_f16 v20, v103, v0, v20
	v_pk_fma_f16 v21, v103, v1, v21
	v_pk_fma_f16 v22, v103, v2, v22
	v_pk_fma_f16 v23, v103, v3, v23
	v_pk_fma_f16 v24, v103, v4, v24
	v_pk_fma_f16 v25, v103, v5, v25
	v_pk_fma_f16 v26, v103, v6, v26
	v_pk_fma_f16 v27, v103, v7, v27
	v_pk_fma_f16 v28, v103, v8, v28
	v_pk_fma_f16 v29, v103, v9, v29
	v_pk_fma_f16 v30, v103, v10, v30
	v_pk_fma_f16 v31, v103, v11, v31
	v_pk_fma_f16 v32, v103, v12, v32
	v_pk_fma_f16 v33, v103, v13, v33
	v_pk_fma_f16 v34, v103, v14, v34
	v_pk_fma_f16 v35, v103, v15, v35
	s_waitcnt vmcnt(6)
	v_cvt_scalef32_pk32_f16_fp6 v[0:15], v[44:49], 1.0
	s_waitcnt lgkmcnt(0)
	v_pk_fma_f16 v20, v16, v0, v20
	v_pk_fma_f16 v21, v16, v1, v21
	v_pk_fma_f16 v22, v16, v2, v22
	v_pk_fma_f16 v23, v16, v3, v23
	v_pk_fma_f16 v24, v16, v4, v24
	v_pk_fma_f16 v25, v16, v5, v25
	v_pk_fma_f16 v26, v16, v6, v26
	v_pk_fma_f16 v27, v16, v7, v27
	v_pk_fma_f16 v28, v16, v8, v28
	v_pk_fma_f16 v29, v16, v9, v29
	v_pk_fma_f16 v30, v16, v10, v30
	v_pk_fma_f16 v31, v16, v11, v31
	v_pk_fma_f16 v32, v16, v12, v32
	v_pk_fma_f16 v33, v16, v13, v33
	v_pk_fma_f16 v34, v16, v14, v34
	v_pk_fma_f16 v16, v16, v15, v35
	s_waitcnt vmcnt(4)
	v_cvt_scalef32_pk32_f16_fp6 v[0:15], v[50:55], 1.0
	v_pk_fma_f16 v20, v17, v0, v20
	v_pk_fma_f16 v21, v17, v1, v21
	v_pk_fma_f16 v22, v17, v2, v22
	v_pk_fma_f16 v23, v17, v3, v23
	v_pk_fma_f16 v24, v17, v4, v24
	v_pk_fma_f16 v25, v17, v5, v25
	v_pk_fma_f16 v26, v17, v6, v26
	v_pk_fma_f16 v27, v17, v7, v27
	v_pk_fma_f16 v28, v17, v8, v28
	v_pk_fma_f16 v29, v17, v9, v29
	v_pk_fma_f16 v30, v17, v10, v30
	v_pk_fma_f16 v31, v17, v11, v31
	v_pk_fma_f16 v32, v17, v12, v32
	v_pk_fma_f16 v33, v17, v13, v33
	v_pk_fma_f16 v34, v17, v14, v34
	v_pk_fma_f16 v35, v17, v15, v16
	s_waitcnt vmcnt(2)
	v_cvt_scalef32_pk32_f16_fp6 v[0:15], v[56:61], 1.0
	v_pk_fma_f16 v36, v18, v0, v20
	v_pk_fma_f16 v37, v18, v1, v21
	v_lshl_add_u64 v[0:1], v[68:69], 2, s[28:29]
	v_lshlrev_b32_e32 v40, 1, v68
	v_add_co_u32_e32 v0, vcc, s27, v0
	global_load_dwordx2 v[16:17], v40, s[22:23]
	s_nop 0
	v_addc_co_u32_e32 v1, vcc, 0, v1, vcc
	v_pk_fma_f16 v38, v18, v2, v22
	v_pk_fma_f16 v39, v18, v3, v23
	global_load_dwordx4 v[20:23], v[0:1], off
	v_pk_fma_f16 v24, v18, v4, v24
	v_pk_fma_f16 v25, v18, v5, v25
	v_pk_fma_f16 v26, v18, v6, v26
	v_pk_fma_f16 v27, v18, v7, v27
	v_pk_fma_f16 v28, v18, v8, v28
	v_pk_fma_f16 v29, v18, v9, v29
	v_pk_fma_f16 v30, v18, v10, v30
	v_pk_fma_f16 v31, v18, v11, v31
	v_pk_fma_f16 v32, v18, v12, v32
	v_pk_fma_f16 v33, v18, v13, v33
	v_pk_fma_f16 v34, v18, v14, v34
	v_pk_fma_f16 v18, v18, v15, v35
	s_waitcnt vmcnt(2)
	v_cvt_scalef32_pk32_f16_fp6 v[0:15], v[62:67], 1.0
	v_pk_fma_f16 v0, v19, v0, v36
	v_pk_fma_f16 v2, v19, v2, v38
	v_pk_fma_f16 v4, v19, v4, v24
	v_pk_fma_f16 v6, v19, v6, v26
	v_pk_fma_f16 v8, v19, v8, v28
	v_pk_fma_f16 v10, v19, v10, v30
	v_pk_fma_f16 v12, v19, v12, v32
	v_pk_fma_f16 v14, v19, v14, v34
	v_permlane32_swap_b32_e32 v0, v8
	v_permlane32_swap_b32_e32 v2, v10
	v_permlane32_swap_b32_e32 v4, v12
	v_permlane32_swap_b32_e32 v6, v14
	v_pk_fma_f16 v1, v19, v1, v37
	v_pk_fma_f16 v3, v19, v3, v39
	v_pk_fma_f16 v5, v19, v5, v25
	v_pk_fma_f16 v7, v19, v7, v27
	v_pk_fma_f16 v9, v19, v9, v29
	v_pk_fma_f16 v11, v19, v11, v31
	v_pk_fma_f16 v13, v19, v13, v33
	v_pk_fma_f16 v15, v19, v15, v18
	v_pk_add_f16 v0, v0, v8
	v_pk_add_f16 v2, v2, v10
	v_pk_add_f16 v4, v4, v12
	v_pk_add_f16 v6, v6, v14
	v_permlane32_swap_b32_e32 v1, v9
	v_permlane32_swap_b32_e32 v3, v11
	v_permlane32_swap_b32_e32 v5, v13
	v_permlane32_swap_b32_e32 v7, v15
	v_permlane16_swap_b32_e32 v0, v4
	v_permlane16_swap_b32_e32 v2, v6
	v_pk_add_f16 v1, v1, v9
	v_pk_add_f16 v3, v3, v11
	v_pk_add_f16 v5, v5, v13
	v_pk_add_f16 v7, v7, v15
	v_pk_add_f16 v0, v0, v4
	v_pk_add_f16 v2, v2, v6
	v_permlane16_swap_b32_e32 v1, v5
	v_permlane16_swap_b32_e32 v3, v7
	v_cndmask_b32_e64 v4, v0, v2, s[2:3]
	v_cndmask_b32_e64 v0, v2, v0, s[2:3]
	v_mov_b32_e32 v2, 0
	v_pk_add_f16 v1, v1, v5
	v_pk_add_f16 v3, v3, v7
	v_mov_b32_dpp v2, v4 row_ror:8 row_mask:0xf bank_mask:0xf
	v_pk_add_f16 v2, v0, v2
	v_cndmask_b32_e64 v0, v1, v3, s[2:3]
	v_cndmask_b32_e64 v1, v3, v1, s[2:3]
	v_mov_b32_e32 v3, 0
	s_andn2_b64 vcc, exec, s[16:17]
	s_waitcnt vmcnt(1)
	v_lshlrev_b32_e32 v4, 16, v16
	v_mov_b32_dpp v3, v0 row_ror:8 row_mask:0xf bank_mask:0xf
	v_pk_add_f16 v3, v1, v3
	v_cvt_f32_f16_e32 v0, v2
	v_cvt_f32_f16_sdwa v1, v2 dst_sel:DWORD dst_unused:UNUSED_PAD src0_sel:WORD_1
	v_cvt_f32_f16_e32 v2, v3
	v_cvt_f32_f16_sdwa v3, v3 dst_sel:DWORD dst_unused:UNUSED_PAD src0_sel:WORD_1
	v_and_b32_e32 v5, 0xffff0000, v16
	v_pk_mul_f32 v[0:1], v[0:1], s[10:11] op_sel_hi:[1,0]
	v_lshlrev_b32_e32 v6, 16, v17
	v_pk_mul_f32 v[2:3], v[2:3], s[10:11] op_sel_hi:[1,0]
	v_and_b32_e32 v7, 0xffff0000, v17
	s_waitcnt vmcnt(0)
	v_pk_fma_f32 v[2:3], v[22:23], v[2:3], v[6:7]
	v_pk_fma_f32 v[0:1], v[20:21], v[0:1], v[4:5]
	s_nop 0
	v_cvt_pk_bf16_f32 v0, v0, v1
	v_cvt_pk_bf16_f32 v1, v2, v3
	global_store_dwordx2 v40, v[0:1], s[22:23]
	s_cbranch_vccnz .LBB0_1501
	s_waitcnt vmcnt(0)
	v_lshlrev_b32_e32 v0, 1, v188
	global_load_dwordx2 v[4:5], v0, s[22:23]
	global_load_dwordx2 v[6:7], v0, s[22:23] offset:512
	global_load_dwordx2 v[8:9], v0, s[22:23] offset:1024
	global_load_dwordx2 v[10:11], v0, s[22:23] offset:1536
	global_load_dwordx2 v[12:13], v0, s[22:23] offset:2048
	global_load_dwordx2 v[14:15], v0, s[22:23] offset:2560
	global_load_dwordx2 v[16:17], v0, s[22:23] offset:3584
	global_load_dwordx2 v[18:19], v0, s[22:23] offset:3072
	v_cmp_lt_i32_e32 vcc, v115, v113
	s_lshl_b64 s[20:21], s[20:21], 11
	s_lshl_b64 s[20:21], s[20:21], 2
	v_cndmask_b32_e32 v0, v111, v115, vcc
	v_lshlrev_b32_e32 v38, 2, v0
	global_load_dwordx4 v[0:3], v[70:71], off
	v_cmp_lt_i32_e32 vcc, v114, v113
	s_add_u32 s20, s80, s20
	s_addc_u32 s21, s81, s21
	s_waitcnt vmcnt(8)
	v_and_b32_e32 v21, 0xffff0000, v4
	s_waitcnt vmcnt(7)
	v_and_b32_e32 v23, 0xffff0000, v6
	v_lshlrev_b32_e32 v20, 16, v4
	v_lshlrev_b32_e32 v22, 16, v6
	s_waitcnt vmcnt(6)
	v_and_b32_e32 v25, 0xffff0000, v8
	v_mul_f32_e32 v39, v21, v21
	v_mul_f32_e32 v40, v23, v23
	v_lshlrev_b32_e32 v4, 16, v5
	v_lshlrev_b32_e32 v6, 16, v7
	v_lshlrev_b32_e32 v24, 16, v8
	s_waitcnt vmcnt(5)
	v_and_b32_e32 v27, 0xffff0000, v10
	v_mul_f32_e32 v41, v25, v25
	v_fmac_f32_e32 v39, v20, v20
	v_fmac_f32_e32 v40, v22, v22
	v_and_b32_e32 v5, 0xffff0000, v5
	v_and_b32_e32 v7, 0xffff0000, v7
	v_lshlrev_b32_e32 v8, 16, v9
	v_lshlrev_b32_e32 v26, 16, v10
	s_waitcnt vmcnt(4)
	v_and_b32_e32 v29, 0xffff0000, v12
	v_mul_f32_e32 v42, v27, v27
	v_fmac_f32_e32 v41, v24, v24
	v_fmac_f32_e32 v39, v4, v4
	v_fmac_f32_e32 v40, v6, v6
	v_and_b32_e32 v9, 0xffff0000, v9
	v_lshlrev_b32_e32 v10, 16, v11
	v_lshlrev_b32_e32 v28, 16, v12
	s_waitcnt vmcnt(3)
	v_and_b32_e32 v31, 0xffff0000, v14
	v_mul_f32_e32 v43, v29, v29
	v_fmac_f32_e32 v42, v26, v26
	v_fmac_f32_e32 v41, v8, v8
	v_fmac_f32_e32 v39, v5, v5
	v_fmac_f32_e32 v40, v7, v7
	v_and_b32_e32 v11, 0xffff0000, v11
	v_lshlrev_b32_e32 v12, 16, v13
	v_lshlrev_b32_e32 v30, 16, v14
	s_waitcnt vmcnt(2)
	v_and_b32_e32 v35, 0xffff0000, v16
	s_waitcnt vmcnt(1)
	v_and_b32_e32 v34, 0xffff0000, v18
	v_mul_f32_e32 v44, v31, v31
	v_fmac_f32_e32 v43, v28, v28
	v_fmac_f32_e32 v42, v10, v10
	v_fmac_f32_e32 v41, v9, v9
	v_add_f32_e32 v39, v39, v40
	v_and_b32_e32 v13, 0xffff0000, v13
	v_lshlrev_b32_e32 v14, 16, v15
	v_lshlrev_b32_e32 v33, 16, v16
	v_lshlrev_b32_e32 v32, 16, v18
	v_lshlrev_b32_e32 v36, 16, v19
	v_and_b32_e32 v16, 0xffff0000, v19
	v_pk_mul_f32 v[18:19], v[34:35], v[34:35]
	v_fmac_f32_e32 v44, v30, v30
	v_fmac_f32_e32 v43, v12, v12
	v_fmac_f32_e32 v42, v11, v11
	v_add_f32_e32 v39, v39, v41
	v_and_b32_e32 v15, 0xffff0000, v15
	v_lshlrev_b32_e32 v37, 16, v17
	v_pk_fma_f32 v[18:19], v[32:33], v[32:33], v[18:19]
	v_fmac_f32_e32 v44, v14, v14
	v_fmac_f32_e32 v43, v13, v13
	v_add_f32_e32 v39, v39, v42
	v_and_b32_e32 v17, 0xffff0000, v17
	v_pk_fma_f32 v[18:19], v[36:37], v[36:37], v[18:19]
	v_fmac_f32_e32 v44, v15, v15
	v_add_f32_e32 v39, v39, v43
	v_pk_fma_f32 v[18:19], v[16:17], v[16:17], v[18:19]
	v_add_f32_e32 v39, v39, v44
	v_add_f32_e32 v18, v39, v18
	v_add_f32_e32 v18, v18, v19
	global_load_dwordx4 v[116:119], v[70:71], off offset:1024
	global_load_dwordx4 v[120:123], v[70:71], off offset:2048
	global_load_dwordx4 v[124:127], v[70:71], off offset:3072
	global_load_dwordx4 v[128:131], v[72:73], off
	global_load_dwordx4 v[132:135], v[74:75], off
	global_load_dwordx4 v[136:139], v[76:77], off
	global_load_dwordx4 v[140:143], v[78:79], off
	ds_bpermute_b32 v19, v38, v18
	v_cndmask_b32_e32 v38, v111, v114, vcc
	v_lshlrev_b32_e32 v38, 2, v38
	v_cmp_lt_i32_e32 vcc, v112, v113
	s_waitcnt lgkmcnt(0)
	v_add_f32_e32 v18, v18, v19
	ds_bpermute_b32 v19, v38, v18
	v_cndmask_b32_e32 v38, v111, v112, vcc
	v_lshlrev_b32_e32 v38, 2, v38
	s_waitcnt lgkmcnt(0)
	v_add_f32_e32 v18, v18, v19
	ds_bpermute_b32 v19, v38, v18
	v_xor_b32_e32 v38, 8, v111
	v_cmp_lt_i32_e32 vcc, v38, v113
	s_waitcnt lgkmcnt(0)
	v_add_f32_e32 v18, v18, v19
	v_cndmask_b32_e32 v38, v111, v38, vcc
	v_lshlrev_b32_e32 v38, 2, v38
	ds_bpermute_b32 v19, v38, v18
	v_xor_b32_e32 v38, 16, v111
	v_cmp_lt_i32_e32 vcc, v38, v113
	s_waitcnt lgkmcnt(0)
	v_add_f32_e32 v18, v18, v19
	v_cndmask_b32_e32 v38, v111, v38, vcc
	v_lshlrev_b32_e32 v38, 2, v38
	ds_bpermute_b32 v19, v38, v18
	v_xor_b32_e32 v38, 32, v111
	v_cmp_lt_i32_e32 vcc, v38, v113
	s_waitcnt lgkmcnt(0)
	v_add_f32_e32 v18, v18, v19
	v_cndmask_b32_e32 v38, v111, v38, vcc
	v_lshlrev_b32_e32 v38, 2, v38
	ds_bpermute_b32 v19, v38, v18
	v_lshlrev_b32_e32 v38, 2, v188
	s_waitcnt lgkmcnt(0)
	v_add_f32_e32 v18, v18, v19
	v_fmamk_f32 v18, v18, 0x3a000000, v91
	v_rsq_f32_e32 v18, v18
	s_nop 0
	v_pk_mul_f32 v[20:21], v[20:21], v[18:19] op_sel_hi:[1,0]
	v_pk_mul_f32 v[4:5], v[4:5], v[18:19] op_sel_hi:[1,0]
	s_waitcnt vmcnt(0)
	v_pk_mul_f32 v[0:1], v[0:1], v[20:21]
	v_pk_mul_f32 v[2:3], v[2:3], v[4:5]
	global_store_dwordx4 v38, v[0:3], s[20:21]
	v_pk_mul_f32 v[4:5], v[6:7], v[18:19] op_sel_hi:[1,0]
	v_pk_mul_f32 v[6:7], v[22:23], v[18:19] op_sel_hi:[1,0]
	v_pk_mul_f32 v[118:119], v[118:119], v[4:5]
	v_pk_mul_f32 v[116:117], v[116:117], v[6:7]
	global_store_dwordx4 v38, v[116:119], s[20:21] offset:1024
	v_pk_mul_f32 v[4:5], v[8:9], v[18:19] op_sel_hi:[1,0]
	v_pk_mul_f32 v[6:7], v[24:25], v[18:19] op_sel_hi:[1,0]
	v_pk_mul_f32 v[122:123], v[122:123], v[4:5]
	v_pk_mul_f32 v[120:121], v[120:121], v[6:7]
	global_store_dwordx4 v38, v[120:123], s[20:21] offset:2048
	v_pk_mul_f32 v[4:5], v[10:11], v[18:19] op_sel_hi:[1,0]
	v_pk_mul_f32 v[6:7], v[26:27], v[18:19] op_sel_hi:[1,0]
	v_pk_mul_f32 v[126:127], v[126:127], v[4:5]
	v_pk_mul_f32 v[124:125], v[124:125], v[6:7]
	global_store_dwordx4 v38, v[124:127], s[20:21] offset:3072
	v_pk_mul_f32 v[4:5], v[12:13], v[18:19] op_sel_hi:[1,0]
	v_pk_mul_f32 v[6:7], v[28:29], v[18:19] op_sel_hi:[1,0]
	v_pk_mul_f32 v[130:131], v[130:131], v[4:5]
	v_pk_mul_f32 v[128:129], v[128:129], v[6:7]
	global_store_dwordx4 v92, v[128:131], s[20:21]
	v_pk_mul_f32 v[4:5], v[14:15], v[18:19] op_sel_hi:[1,0]
	v_pk_mul_f32 v[6:7], v[30:31], v[18:19] op_sel_hi:[1,0]
	v_pk_mul_f32 v[134:135], v[134:135], v[4:5]
	v_pk_mul_f32 v[132:133], v[132:133], v[6:7]
	global_store_dwordx4 v93, v[132:135], s[20:21]
	v_mov_b32_e32 v4, v36
	v_mov_b32_e32 v5, v16
	v_mov_b32_e32 v6, v32
	v_mov_b32_e32 v7, v34
	v_pk_mul_f32 v[4:5], v[4:5], v[18:19] op_sel_hi:[1,0]
	v_pk_mul_f32 v[6:7], v[6:7], v[18:19] op_sel_hi:[1,0]
	v_mov_b32_e32 v34, v33
	v_mov_b32_e32 v16, v37
	v_pk_mul_f32 v[136:137], v[6:7], v[136:137]
	v_pk_mul_f32 v[138:139], v[4:5], v[138:139]
	global_store_dwordx4 v94, v[136:139], s[20:21]
	v_pk_mul_f32 v[4:5], v[16:17], v[18:19] op_sel_hi:[1,0]
	v_pk_mul_f32 v[6:7], v[34:35], v[18:19] op_sel_hi:[1,0]
	v_pk_mul_f32 v[142:143], v[4:5], v[142:143]
	v_pk_mul_f32 v[140:141], v[6:7], v[140:141]
	global_store_dwordx4 v95, v[140:143], s[20:21]
	s_branch .LBB0_1501
